# out-projection EpiResid epilogue: residual loads of all 8 accumulator rows issued up front (dead fragment regs), gMLP u/bias loads hoisted to iteration top, m0 save/restore trims in fp8 GEMM DMA block
# speedup vs baseline: 1.0120x; 1.0041x over previous
.LBB0_350:
	s_waitcnt vmcnt(0)
	v_lshl_add_u64 v[18:19], v[48:49], 0, s[30:31]
	v_readlane_b32 s72, v254, 4
	v_readlane_b32 s80, v254, 12
	v_readlane_b32 s81, v254, 13
	v_mov_b32_e32 v31, v8
	v_mov_b32_e32 v8, v7
	s_nop 0
	v_mov_b32_e32 v30, v6
	v_mov_b32_e32 v6, v2
	v_mov_b32_e32 v7, v4
	v_mov_b32_e32 v4, v3
	v_mov_b32_e32 v2, v14
	v_mov_b32_e32 v3, v16
	v_mov_b32_e32 v16, v15
	v_mov_b32_e32 v14, v10
	v_mov_b32_e32 v15, v12
	v_mov_b32_e32 v12, v11
	s_add_u32 s30, s30, 0x80
	s_addc_u32 s31, s31, 0
	s_cmpk_eq_i32 s30, 0x200
	v_readlane_b32 s73, v254, 5
	v_readlane_b32 s74, v254, 6
	v_readlane_b32 s75, v254, 7
	v_readlane_b32 s76, v254, 8
	v_readlane_b32 s77, v254, 9
	v_readlane_b32 s78, v254, 10
	v_readlane_b32 s79, v254, 11
	v_readlane_b32 s82, v254, 14
	v_readlane_b32 s83, v254, 15
	v_readlane_b32 s84, v254, 16
	v_readlane_b32 s85, v254, 17
	v_readlane_b32 s86, v254, 18
	v_readlane_b32 s87, v254, 19
	s_waitcnt vmcnt(4)
	v_lshlrev_b32_e32 v11, 16, v89
	v_lshlrev_b32_e32 v10, 16, v88
	v_and_b32_e32 v89, 0xffff0000, v89
	v_and_b32_e32 v88, 0xffff0000, v88
	s_waitcnt vmcnt(3)
	v_pk_add_f32 v[8:9], v[96:97], v[8:9] op_sel_hi:[0,1]
	v_pk_add_f32 v[30:31], v[96:97], v[30:31] op_sel_hi:[0,1]
	s_waitcnt vmcnt(2)
	v_lshlrev_b32_e32 v33, 16, v91
	v_lshlrev_b32_e32 v32, 16, v90
	v_and_b32_e32 v91, 0xffff0000, v91
	v_and_b32_e32 v90, 0xffff0000, v90
	v_pk_add_f32 v[4:5], v[96:97], v[4:5] op_sel_hi:[0,1]
	s_waitcnt vmcnt(1)
	v_lshlrev_b32_e32 v35, 16, v93
	v_lshlrev_b32_e32 v34, 16, v92
	v_pk_add_f32 v[2:3], v[96:97], v[2:3] op_sel_hi:[0,1]
	v_and_b32_e32 v93, 0xffff0000, v93
	v_and_b32_e32 v92, 0xffff0000, v92
	v_pk_add_f32 v[16:17], v[96:97], v[16:17] op_sel_hi:[0,1]
	v_pk_mul_f32 v[8:9], v[8:9], v[88:89]
	v_pk_add_f32 v[6:7], v[96:97], v[6:7] op_sel_hi:[0,1]
	v_pk_add_f32 v[14:15], v[96:97], v[14:15] op_sel_hi:[0,1]
	v_pk_mul_f32 v[10:11], v[30:31], v[10:11]
	v_pk_mul_f32 v[4:5], v[4:5], v[90:91]
	v_pk_mul_f32 v[2:3], v[2:3], v[34:35]
	v_pk_mul_f32 v[16:17], v[16:17], v[92:93]
	v_and_b32_sdwa v97, v9, v60 dst_sel:DWORD dst_unused:UNUSED_PAD src0_sel:WORD_1 src1_sel:DWORD
	v_and_b32_sdwa v90, v8, v60 dst_sel:DWORD dst_unused:UNUSED_PAD src0_sel:WORD_1 src1_sel:DWORD
	v_pk_mul_f32 v[6:7], v[6:7], v[32:33]
	v_and_b32_sdwa v88, v11, v60 dst_sel:DWORD dst_unused:UNUSED_PAD src0_sel:WORD_1 src1_sel:DWORD
	v_and_b32_sdwa v89, v10, v60 dst_sel:DWORD dst_unused:UNUSED_PAD src0_sel:WORD_1 src1_sel:DWORD
	v_and_b32_sdwa v93, v5, v60 dst_sel:DWORD dst_unused:UNUSED_PAD src0_sel:WORD_1 src1_sel:DWORD
	v_and_b32_sdwa v30, v4, v60 dst_sel:DWORD dst_unused:UNUSED_PAD src0_sel:WORD_1 src1_sel:DWORD
	v_and_b32_sdwa v31, v3, v60 dst_sel:DWORD dst_unused:UNUSED_PAD src0_sel:WORD_1 src1_sel:DWORD
	v_and_b32_sdwa v32, v2, v60 dst_sel:DWORD dst_unused:UNUSED_PAD src0_sel:WORD_1 src1_sel:DWORD
	v_and_b32_sdwa v33, v17, v60 dst_sel:DWORD dst_unused:UNUSED_PAD src0_sel:WORD_1 src1_sel:DWORD
	v_and_b32_sdwa v34, v16, v60 dst_sel:DWORD dst_unused:UNUSED_PAD src0_sel:WORD_1 src1_sel:DWORD
	v_add3_u32 v9, v9, v97, s37
	v_add3_u32 v8, v8, v90, s37
	v_and_b32_sdwa v91, v7, v60 dst_sel:DWORD dst_unused:UNUSED_PAD src0_sel:WORD_1 src1_sel:DWORD
	v_and_b32_sdwa v92, v6, v60 dst_sel:DWORD dst_unused:UNUSED_PAD src0_sel:WORD_1 src1_sel:DWORD
	v_add3_u32 v10, v10, v89, s37
	v_add3_u32 v11, v11, v88, s37
	v_add3_u32 v5, v5, v93, s37
	v_add3_u32 v4, v4, v30, s37
	v_add3_u32 v88, v2, v32, s37
	v_add3_u32 v89, v3, v31, s37
	v_add3_u32 v2, v17, v33, s37
	v_add3_u32 v3, v16, v34, s37
	v_and_b32_e32 v9, 0xffff0000, v9
	v_and_b32_e32 v8, 0xffff0000, v8
	v_add3_u32 v6, v6, v92, s37
	v_add3_u32 v7, v7, v91, s37
	v_and_b32_e32 v5, 0xffff0000, v5
	v_and_b32_e32 v4, 0xffff0000, v4
	v_and_b32_e32 v16, 0xffff0000, v2
	v_and_b32_e32 v17, 0xffff0000, v3
	v_or_b32_sdwa v3, v9, v11 dst_sel:DWORD dst_unused:UNUSED_PAD src0_sel:DWORD src1_sel:WORD_1
	v_or_b32_sdwa v2, v8, v10 dst_sel:DWORD dst_unused:UNUSED_PAD src0_sel:DWORD src1_sel:WORD_1
	s_waitcnt vmcnt(0)
	v_lshlrev_b32_e32 v37, 16, v95
	v_lshlrev_b32_e32 v36, 16, v94
	v_and_b32_e32 v95, 0xffff0000, v95
	v_and_b32_e32 v94, 0xffff0000, v94
	v_or_b32_sdwa v5, v5, v7 dst_sel:DWORD dst_unused:UNUSED_PAD src0_sel:DWORD src1_sel:WORD_1
	v_or_b32_sdwa v4, v4, v6 dst_sel:DWORD dst_unused:UNUSED_PAD src0_sel:DWORD src1_sel:WORD_1
	v_or_b32_sdwa v7, v16, v89 dst_sel:DWORD dst_unused:UNUSED_PAD src0_sel:DWORD src1_sel:WORD_1
	v_or_b32_sdwa v6, v17, v88 dst_sel:DWORD dst_unused:UNUSED_PAD src0_sel:DWORD src1_sel:WORD_1
	global_store_dwordx2 v[18:19], v[2:3], off offset:-64
	global_store_dwordx2 v[18:19], v[4:5], off offset:-32
	global_store_dwordx2 v[18:19], v[6:7], off
	v_pk_add_f32 v[2:3], v[96:97], v[12:13] op_sel_hi:[0,1]
	v_pk_mul_f32 v[2:3], v[2:3], v[94:95]
	v_pk_mul_f32 v[14:15], v[14:15], v[36:37]
	v_and_b32_sdwa v6, v3, v60 dst_sel:DWORD dst_unused:UNUSED_PAD src0_sel:WORD_1 src1_sel:DWORD
	v_and_b32_sdwa v7, v2, v60 dst_sel:DWORD dst_unused:UNUSED_PAD src0_sel:WORD_1 src1_sel:DWORD
	v_and_b32_sdwa v4, v15, v60 dst_sel:DWORD dst_unused:UNUSED_PAD src0_sel:WORD_1 src1_sel:DWORD
	v_and_b32_sdwa v5, v14, v60 dst_sel:DWORD dst_unused:UNUSED_PAD src0_sel:WORD_1 src1_sel:DWORD
	v_add3_u32 v3, v3, v6, s37
	v_add3_u32 v2, v2, v7, s37
	v_add3_u32 v5, v14, v5, s37
	v_add3_u32 v4, v15, v4, s37
	v_and_b32_e32 v3, 0xffff0000, v3
	v_and_b32_e32 v2, 0xffff0000, v2
	v_or_b32_sdwa v3, v3, v4 dst_sel:DWORD dst_unused:UNUSED_PAD src0_sel:DWORD src1_sel:WORD_1
	v_or_b32_sdwa v2, v2, v5 dst_sel:DWORD dst_unused:UNUSED_PAD src0_sel:DWORD src1_sel:WORD_1
	global_store_dwordx2 v[18:19], v[2:3], off offset:32
	s_cbranch_scc1 .LBB0_368
.LBB0_351:
	v_lshl_add_u64 v[6:7], v[46:47], 0, s[30:31]
	v_add_co_u32_e32 v2, vcc, 0x10a00000, v6
	s_nop 1
	v_addc_co_u32_e32 v3, vcc, 0, v7, vcc
	s_barrier
	global_load_dwordx4 v[2:5], v[2:3], off offset:512
	v_lshl_add_u64 v[6:7], v[6:7], 0, s[34:35]
	global_load_dwordx4 v[6:9], v[6:7], off offset:16
	v_add_u32_e32 v50, s30, v44
	v_ashrrev_i32_e32 v51, 31, v50
	v_lshl_add_u64 v[98:99], v[48:49], 0, s[30:31]
	v_readlane_b32 s100, v254, 12
	v_readlane_b32 s101, v254, 13
	global_load_dwordx2 v[88:89], v[98:99], off offset:-64
	global_load_dwordx2 v[90:91], v[98:99], off offset:-32
	global_load_dwordx2 v[92:93], v[98:99], off
	global_load_dwordx2 v[94:95], v[98:99], off offset:32
	v_lshl_add_u64 v[96:97], v[50:51], 2, s[100:101]
	global_load_dword v96, v[96:97], off
	s_waitcnt vmcnt(6)
	v_lshlrev_b32_e32 v10, 16, v2
	v_and_b32_e32 v2, 0xffff0000, v2
	v_add_f32_e32 v18, 0, v10
	v_lshlrev_b32_e32 v11, 16, v3
	v_add_f32_e32 v18, v18, v2
	v_and_b32_e32 v3, 0xffff0000, v3
	v_add_f32_e32 v18, v18, v11
	v_lshlrev_b32_e32 v12, 16, v4
	v_add_f32_e32 v18, v18, v3
	v_and_b32_e32 v4, 0xffff0000, v4
	v_add_f32_e32 v18, v18, v12
	v_lshlrev_b32_e32 v13, 16, v5
	v_add_f32_e32 v18, v18, v4
	v_and_b32_e32 v5, 0xffff0000, v5
	v_add_f32_e32 v18, v18, v13
	s_waitcnt vmcnt(5)
	v_lshlrev_b32_e32 v14, 16, v6
	v_add_f32_e32 v18, v18, v5
	v_and_b32_e32 v6, 0xffff0000, v6
	v_add_f32_e32 v18, v18, v14
	v_lshlrev_b32_e32 v15, 16, v7
	v_add_f32_e32 v18, v18, v6
	v_and_b32_e32 v7, 0xffff0000, v7
	v_add_f32_e32 v18, v18, v15
	v_lshlrev_b32_e32 v16, 16, v8
	v_add_f32_e32 v18, v18, v7
	v_and_b32_e32 v8, 0xffff0000, v8
	v_add_f32_e32 v18, v18, v16
	v_lshlrev_b32_e32 v17, 16, v9
	v_add_f32_e32 v18, v18, v8
	v_and_b32_e32 v9, 0xffff0000, v9
	v_add_f32_e32 v18, v18, v17
	v_add_f32_e32 v18, v18, v9
	s_waitcnt lgkmcnt(0)
	s_nop 1
	v_add_f32_dpp v18, v18, v18 quad_perm:[1,0,3,2] row_mask:0xf bank_mask:0xf
	s_nop 1
	v_add_f32_dpp v18, v18, v18 quad_perm:[2,3,0,1] row_mask:0xf bank_mask:0xf
	v_fmac_f32_e32 v2, 0xbc800000, v18
	v_fmac_f32_e32 v10, 0xbc800000, v18
	v_fmac_f32_e32 v11, 0xbc800000, v18
	v_fmac_f32_e32 v3, 0xbc800000, v18
	v_fmac_f32_e32 v12, 0xbc800000, v18
	v_fmac_f32_e32 v4, 0xbc800000, v18
	v_fmac_f32_e32 v13, 0xbc800000, v18
	v_fmac_f32_e32 v5, 0xbc800000, v18
	v_fmac_f32_e32 v14, 0xbc800000, v18
	v_fmac_f32_e32 v6, 0xbc800000, v18
	v_fmac_f32_e32 v15, 0xbc800000, v18
	v_fmac_f32_e32 v7, 0xbc800000, v18
	v_fmac_f32_e32 v16, 0xbc800000, v18
	v_fmac_f32_e32 v8, 0xbc800000, v18
	v_fmac_f32_e32 v17, 0xbc800000, v18
	v_fmac_f32_e32 v9, 0xbc800000, v18
	v_mul_f32_e32 v18, v2, v2
	v_fmac_f32_e32 v18, v10, v10
	v_fmac_f32_e32 v18, v11, v11
	v_fmac_f32_e32 v18, v3, v3
	v_fmac_f32_e32 v18, v12, v12
	v_fmac_f32_e32 v18, v4, v4
	v_fmac_f32_e32 v18, v13, v13
	v_fmac_f32_e32 v18, v5, v5
	v_fmac_f32_e32 v18, v14, v14
	v_fmac_f32_e32 v18, v6, v6
	v_fmac_f32_e32 v18, v15, v15
	v_fmac_f32_e32 v18, v7, v7
	v_fmac_f32_e32 v18, v16, v16
	v_fmac_f32_e32 v18, v8, v8
	v_fmac_f32_e32 v18, v17, v17
	v_fmac_f32_e32 v18, v9, v9
	s_waitcnt lgkmcnt(0)
	s_nop 1
	v_add_f32_dpp v18, v18, v18 quad_perm:[1,0,3,2] row_mask:0xf bank_mask:0xf
	s_nop 1
	v_add_f32_dpp v18, v18, v18 quad_perm:[2,3,0,1] row_mask:0xf bank_mask:0xf
	v_fmamk_f32 v18, v18, 0x3c800000, v39
	v_mul_f32_e32 v19, 0x4f800000, v18
	v_cmp_gt_f32_e32 vcc, s33, v18
	s_nop 1
	v_cndmask_b32_e32 v18, v18, v19, vcc
	v_sqrt_f32_e32 v19, v18
	s_nop 0
	v_add_u32_e32 v20, -1, v19
	v_add_u32_e32 v21, 1, v19
	v_fma_f32 v22, -v20, v19, v18
	v_fma_f32 v23, -v21, v19, v18
	v_cmp_ge_f32_e64 s[0:1], 0, v22
	s_nop 1
	v_cndmask_b32_e64 v19, v19, v20, s[0:1]
	v_cmp_lt_f32_e64 s[0:1], 0, v23
	s_nop 1
	v_cndmask_b32_e64 v19, v19, v21, s[0:1]
	v_mul_f32_e32 v20, 0x37800000, v19
	v_cndmask_b32_e32 v19, v19, v20, vcc
	v_cmp_class_f32_e32 vcc, v18, v54
	s_nop 1
	v_cndmask_b32_e32 v18, v19, v18, vcc
	v_div_scale_f32 v19, s[0:1], v18, v18, 1.0
	v_rcp_f32_e32 v20, v19
	v_div_scale_f32 v21, vcc, 1.0, v18, 1.0
	v_fma_f32 v22, -v19, v20, 1.0
	v_fmac_f32_e32 v20, v22, v20
	v_mul_f32_e32 v22, v21, v20
	v_fma_f32 v23, -v19, v22, v21
	v_fmac_f32_e32 v22, v23, v20
	v_fma_f32 v19, -v19, v22, v21
	v_div_fmas_f32 v19, v19, v20, v22
	v_div_fixup_f32 v18, v19, v18, 1.0
	v_mul_f32_e32 v10, v10, v18
	v_mul_f32_e32 v2, v2, v18
	v_mul_f32_e32 v11, v11, v18
	v_mul_f32_e32 v3, v3, v18
	v_mul_f32_e32 v12, v12, v18
	v_mul_f32_e32 v4, v4, v18
	v_mul_f32_e32 v13, v13, v18
	v_mul_f32_e32 v5, v5, v18
	v_mul_f32_e32 v14, v14, v18
	v_mul_f32_e32 v6, v6, v18
	v_mul_f32_e32 v15, v15, v18
	v_mul_f32_e32 v7, v7, v18
	v_mul_f32_e32 v16, v16, v18
	v_mul_f32_e32 v8, v8, v18
	v_bfe_u32 v19, v10, 16, 1
	v_bfe_u32 v20, v2, 16, 1
	v_mul_f32_e32 v17, v17, v18
	v_bfe_u32 v21, v11, 16, 1
	v_bfe_u32 v22, v3, 16, 1
	v_bfe_u32 v23, v12, 16, 1
	v_bfe_u32 v24, v4, 16, 1
	v_bfe_u32 v25, v13, 16, 1
	v_bfe_u32 v26, v5, 16, 1
	v_bfe_u32 v27, v14, 16, 1
	v_bfe_u32 v28, v6, 16, 1
	v_bfe_u32 v29, v15, 16, 1
	v_bfe_u32 v30, v7, 16, 1
	v_bfe_u32 v31, v16, 16, 1
	v_bfe_u32 v32, v8, 16, 1
	v_add3_u32 v10, v10, v19, s37
	v_add3_u32 v2, v2, v20, s37
	v_add3_u32 v11, v11, v21, s37
	v_add3_u32 v3, v3, v22, s37
	v_add3_u32 v12, v12, v23, s37
	v_add3_u32 v4, v4, v24, s37
	v_add3_u32 v13, v13, v25, s37
	v_add3_u32 v5, v5, v26, s37
	v_add3_u32 v14, v14, v27, s37
	v_add3_u32 v6, v6, v28, s37
	v_add3_u32 v15, v15, v29, s37
	v_add3_u32 v7, v7, v30, s37
	v_add3_u32 v16, v16, v31, s37
	v_add3_u32 v8, v8, v32, s37
	ds_write_b16_d16_hi v56, v10
	ds_write_b16_d16_hi v56, v2 offset:272
	ds_write_b16_d16_hi v56, v11 offset:544
	ds_write_b16_d16_hi v56, v3 offset:816
	ds_write_b16_d16_hi v56, v12 offset:1088
	ds_write_b16_d16_hi v56, v4 offset:1360
	ds_write_b16_d16_hi v56, v13 offset:1632
	ds_write_b16_d16_hi v56, v5 offset:1904
	ds_write_b16_d16_hi v56, v14 offset:2176
	ds_write_b16_d16_hi v56, v6 offset:2448
	ds_write_b16_d16_hi v56, v15 offset:2720
	ds_write_b16_d16_hi v56, v7 offset:2992
	ds_write_b16_d16_hi v56, v16 offset:3264
	ds_write_b16_d16_hi v56, v8 offset:3536
	v_bfe_u32 v2, v17, 16, 1
	v_add3_u32 v2, v17, v2, s37
	ds_write_b16_d16_hi v56, v2 offset:3808
	v_mul_f32_e32 v2, v9, v18
	v_bfe_u32 v3, v2, 16, 1
	v_add3_u32 v2, v2, v3, s37
	ds_write_b16_d16_hi v56, v2 offset:4080
	v_lshlrev_b64 v[2:3], 8, v[50:51]
	s_and_b64 vcc, exec, s[2:3]
	v_lshl_add_u64 v[2:3], v[42:43], 0, v[2:3]
	s_cbranch_vccnz .LBB0_356
	global_load_dwordx4 v[30:33], v[2:3], off
	v_cndmask_b32_e64 v4, 0, 1, s[24:25]
	v_cmp_ne_u32_e64 s[8:9], 1, v4
	s_andn2_b64 vcc, exec, s[24:25]
	s_cbranch_vccz .LBB0_357

.LBB0_595:
	v_lshl_add_u32 v146, s38, 8, v152
	s_lshl_b32 s26, s55, 8
	s_ashr_i32 s27, s26, 31
	v_ashrrev_i32_e32 v147, 31, v146
	v_lshl_add_u64 v[144:145], s[26:27], 1, v[138:139]
	v_lshlrev_b64 v[148:149], 11, v[146:147]
	v_lshl_add_u64 v[150:151], v[144:145], 0, v[148:149]
	global_load_dwordx4 v[156:159], v[150:151], off
	global_load_dwordx4 v[160:163], v[150:151], off offset:256
	v_or_b32_e32 v148, 16, v146
	v_ashrrev_i32_e32 v149, 31, v148
	v_lshlrev_b64 v[148:149], 11, v[148:149]
	v_lshl_add_u64 v[148:149], v[144:145], 0, v[148:149]
	global_load_dwordx4 v[164:167], v[148:149], off
	global_load_dwordx4 v[168:171], v[148:149], off offset:256
	v_or_b32_e32 v242, 32, v146
	v_ashrrev_i32_e32 v243, 31, v242
	v_lshlrev_b64 v[242:243], 11, v[242:243]
	v_lshl_add_u64 v[242:243], v[144:145], 0, v[242:243]
	global_load_dwordx4 v[184:187], v[242:243], off
	global_load_dwordx4 v[188:191], v[242:243], off offset:256
	v_or_b32_e32 v244, 48, v146
	v_ashrrev_i32_e32 v245, 31, v244
	v_lshlrev_b64 v[244:245], 11, v[244:245]
	v_lshl_add_u64 v[244:245], v[144:145], 0, v[244:245]
	global_load_dwordx4 v[192:195], v[244:245], off
	global_load_dwordx4 v[196:199], v[244:245], off offset:256
	v_add_u32_e32 v246, 0x80, v146
	v_ashrrev_i32_e32 v247, 31, v246
	v_lshlrev_b64 v[246:247], 11, v[246:247]
	v_lshl_add_u64 v[246:247], v[144:145], 0, v[246:247]
	global_load_dwordx4 v[200:203], v[246:247], off
	global_load_dwordx4 v[204:207], v[246:247], off offset:256
	v_add_u32_e32 v248, 0x90, v146
	v_ashrrev_i32_e32 v249, 31, v248
	v_lshlrev_b64 v[248:249], 11, v[248:249]
	v_lshl_add_u64 v[248:249], v[144:145], 0, v[248:249]
	global_load_dwordx4 v[208:211], v[248:249], off
	global_load_dwordx4 v[222:225], v[248:249], off offset:256
	v_add_u32_e32 v250, 0xa0, v146
	v_ashrrev_i32_e32 v251, 31, v250
	v_lshlrev_b64 v[250:251], 11, v[250:251]
	v_lshl_add_u64 v[250:251], v[144:145], 0, v[250:251]
	global_load_dwordx4 v[226:229], v[250:251], off
	global_load_dwordx4 v[230:233], v[250:251], off offset:256
	v_add_u32_e32 v252, 0xb0, v146
	v_ashrrev_i32_e32 v253, 31, v252
	v_lshlrev_b64 v[252:253], 11, v[252:253]
	v_lshl_add_u64 v[252:253], v[144:145], 0, v[252:253]
	global_load_dwordx4 v[234:237], v[252:253], off
	global_load_dwordx4 v[238:241], v[252:253], off offset:256
	v_or_b32_e32 v172, 32, v146
	s_and_b64 vcc, exec, s[2:3]
	s_mov_b64 s[2:3], -1
	s_waitcnt vmcnt(12)
	v_lshlrev_b32_e32 v174, 16, v156
	v_and_b32_e32 v175, 0xffff0000, v156
	v_lshlrev_b32_e32 v156, 16, v157
	v_and_b32_e32 v157, 0xffff0000, v157
	v_lshlrev_b32_e32 v176, 16, v158
	v_and_b32_e32 v177, 0xffff0000, v158
	v_lshlrev_b32_e32 v158, 16, v159
	v_and_b32_e32 v159, 0xffff0000, v159
	v_lshlrev_b32_e32 v178, 16, v160
	v_and_b32_e32 v179, 0xffff0000, v160
	v_lshlrev_b32_e32 v160, 16, v161
	v_and_b32_e32 v161, 0xffff0000, v161
	v_lshlrev_b32_e32 v180, 16, v162
	v_and_b32_e32 v181, 0xffff0000, v162
	v_lshlrev_b32_e32 v162, 16, v163
	v_and_b32_e32 v163, 0xffff0000, v163
	v_pk_fma_f32 v[128:129], v[156:157], s[20:21], v[128:129] op_sel_hi:[1,0,1]
	v_pk_fma_f32 v[126:127], v[174:175], s[20:21], v[126:127] op_sel_hi:[1,0,1]
	v_pk_fma_f32 v[124:125], v[158:159], s[20:21], v[124:125] op_sel_hi:[1,0,1]
	v_pk_fma_f32 v[122:123], v[176:177], s[20:21], v[122:123] op_sel_hi:[1,0,1]
	v_pk_fma_f32 v[120:121], v[160:161], s[20:21], v[120:121] op_sel_hi:[1,0,1]
	v_pk_fma_f32 v[118:119], v[178:179], s[20:21], v[118:119] op_sel_hi:[1,0,1]
	v_pk_fma_f32 v[116:117], v[162:163], s[20:21], v[116:117] op_sel_hi:[1,0,1]
	v_pk_fma_f32 v[114:115], v[180:181], s[20:21], v[114:115] op_sel_hi:[1,0,1]
	v_bfe_u32 v147, v126, 16, 1
	v_bfe_u32 v158, v128, 16, 1
	v_bfe_u32 v157, v127, 16, 1
	v_bfe_u32 v159, v129, 16, 1
	v_bfe_u32 v173, v118, 16, 1
	v_bfe_u32 v175, v120, 16, 1
	v_bfe_u32 v177, v114, 16, 1
	v_bfe_u32 v178, v115, 16, 1
	v_bfe_u32 v179, v116, 16, 1
	v_bfe_u32 v180, v117, 16, 1
	v_add3_u32 v126, v126, v147, s51
	v_add3_u32 v128, v128, v158, s51
	v_bfe_u32 v174, v119, 16, 1
	v_bfe_u32 v176, v121, 16, 1
	v_add3_u32 v127, v127, v157, s51
	v_add3_u32 v129, v129, v159, s51
	v_add3_u32 v118, v118, v173, s51
	v_add3_u32 v120, v120, v175, s51
	v_add3_u32 v114, v114, v177, s51
	v_add3_u32 v147, v115, v178, s51
	v_add3_u32 v115, v116, v179, s51
	v_add3_u32 v157, v117, v180, s51
	v_lshrrev_b32_e32 v116, 16, v126
	v_lshrrev_b32_e32 v117, 16, v128
	v_add3_u32 v119, v119, v174, s51
	v_add3_u32 v121, v121, v176, s51
	v_lshrrev_b32_e32 v118, 16, v118
	v_lshrrev_b32_e32 v120, 16, v120
	v_lshrrev_b32_e32 v126, 16, v114
	v_lshrrev_b32_e32 v128, 16, v115
	v_and_or_b32 v114, v127, s50, v116
	v_and_or_b32 v115, v129, s50, v117
	v_cvt_pk_bf16_f32 v116, v122, v123
	v_cvt_pk_bf16_f32 v117, v124, v125
	v_ashrrev_i32_e32 v173, 31, v172
	v_and_or_b32 v118, v119, s50, v118
	v_and_or_b32 v119, v121, s50, v120
	v_and_or_b32 v120, v147, s50, v126
	v_and_or_b32 v121, v157, s50, v128
	global_store_dwordx4 v[150:151], v[114:117], off
	global_store_dwordx4 v[150:151], v[118:121], off offset:256
	v_lshlrev_b32_e32 v156, 16, v164
	v_lshlrev_b64 v[114:115], 11, v[172:173]
	v_lshl_add_u64 v[114:115], v[144:145], 0, v[114:115]
	v_and_b32_e32 v157, 0xffff0000, v164
	v_lshlrev_b32_e32 v124, 16, v165
	v_and_b32_e32 v125, 0xffff0000, v165
	v_lshlrev_b32_e32 v126, 16, v166
	v_and_b32_e32 v127, 0xffff0000, v166
	v_lshlrev_b32_e32 v128, 16, v167
	v_and_b32_e32 v129, 0xffff0000, v167
	v_pk_fma_f32 v[110:111], v[156:157], s[20:21], v[110:111] op_sel_hi:[1,0,1]
	v_pk_fma_f32 v[112:113], v[124:125], s[20:21], v[112:113] op_sel_hi:[1,0,1]
	v_pk_fma_f32 v[124:125], v[128:129], s[20:21], v[108:109] op_sel_hi:[1,0,1]
	v_pk_fma_f32 v[108:109], v[126:127], s[20:21], v[106:107] op_sel_hi:[1,0,1]
	v_cvt_pk_bf16_f32 v106, v110, v111
	v_cvt_pk_bf16_f32 v107, v112, v113
	v_cvt_pk_bf16_f32 v108, v108, v109
	v_lshlrev_b32_e32 v150, 16, v168
	v_and_b32_e32 v151, 0xffff0000, v168
	v_lshlrev_b32_e32 v162, 16, v171
	v_and_b32_e32 v163, 0xffff0000, v171
	v_cvt_pk_bf16_f32 v109, v124, v125
	v_pk_fma_f32 v[102:103], v[150:151], s[20:21], v[102:103] op_sel_hi:[1,0,1]
	global_store_dwordx4 v[148:149], v[106:109], off
	v_lshlrev_b32_e32 v158, 16, v169
	v_and_b32_e32 v159, 0xffff0000, v169
	v_pk_fma_f32 v[108:109], v[162:163], s[20:21], v[100:101] op_sel_hi:[1,0,1]
	v_pk_fma_f32 v[104:105], v[158:159], s[20:21], v[104:105] op_sel_hi:[1,0,1]
	v_cvt_pk_bf16_f32 v100, v102, v103
	v_lshlrev_b32_e32 v160, 16, v170
	v_and_b32_e32 v161, 0xffff0000, v170
	v_pk_fma_f32 v[98:99], v[160:161], s[20:21], v[98:99] op_sel_hi:[1,0,1]
	v_cvt_pk_bf16_f32 v101, v104, v105
	v_cvt_pk_bf16_f32 v102, v98, v99
	v_bfe_u32 v98, v108, 16, 1
	v_add3_u32 v98, v108, v98, s51
	v_lshrrev_b32_e32 v103, 16, v98
	v_or_b32_e32 v98, 48, v146
	v_ashrrev_i32_e32 v99, 31, v98
	v_lshlrev_b64 v[98:99], 11, v[98:99]
	v_lshl_add_u64 v[98:99], v[144:145], 0, v[98:99]
	v_bfe_u32 v108, v109, 16, 1
	v_add3_u32 v108, v109, v108, s51
	v_and_or_b32 v103, v108, s50, v103
	global_store_dwordx4 v[148:149], v[100:103], off offset:256
	s_waitcnt vmcnt(14)
	v_lshlrev_b32_e32 v108, 16, v184
	v_and_b32_e32 v109, 0xffff0000, v184
	v_lshlrev_b32_e32 v110, 16, v185
	v_and_b32_e32 v111, 0xffff0000, v185
	v_lshlrev_b32_e32 v112, 16, v186
	v_and_b32_e32 v113, 0xffff0000, v186
	v_lshlrev_b32_e32 v116, 16, v187
	v_and_b32_e32 v117, 0xffff0000, v187
	v_pk_fma_f32 v[94:95], v[108:109], s[20:21], v[94:95] op_sel_hi:[1,0,1]
	v_pk_fma_f32 v[108:109], v[116:117], s[20:21], v[92:93] op_sel_hi:[1,0,1]
	v_pk_fma_f32 v[92:93], v[112:113], s[20:21], v[90:91] op_sel_hi:[1,0,1]
	v_pk_fma_f32 v[96:97], v[110:111], s[20:21], v[96:97] op_sel_hi:[1,0,1]
	v_cvt_pk_bf16_f32 v90, v94, v95
	v_cvt_pk_bf16_f32 v91, v96, v97
	v_cvt_pk_bf16_f32 v92, v92, v93
	s_waitcnt vmcnt(14)
	v_lshlrev_b32_e32 v118, 16, v188
	v_and_b32_e32 v119, 0xffff0000, v188
	v_lshlrev_b32_e32 v124, 16, v190
	v_and_b32_e32 v125, 0xffff0000, v190
	v_lshlrev_b32_e32 v122, 16, v191
	v_and_b32_e32 v123, 0xffff0000, v191
	v_cvt_pk_bf16_f32 v93, v108, v109
	v_pk_fma_f32 v[86:87], v[118:119], s[20:21], v[86:87] op_sel_hi:[1,0,1]
	global_store_dwordx4 v[114:115], v[90:93], off
	v_lshlrev_b32_e32 v120, 16, v189
	v_and_b32_e32 v121, 0xffff0000, v189
	v_pk_fma_f32 v[90:91], v[122:123], s[20:21], v[84:85] op_sel_hi:[1,0,1]
	v_pk_fma_f32 v[84:85], v[124:125], s[20:21], v[82:83] op_sel_hi:[1,0,1]
	v_pk_fma_f32 v[88:89], v[120:121], s[20:21], v[88:89] op_sel_hi:[1,0,1]
	v_cvt_pk_bf16_f32 v82, v86, v87
	v_cvt_pk_bf16_f32 v83, v88, v89
	v_cvt_pk_bf16_f32 v84, v84, v85
	v_cvt_pk_bf16_f32 v85, v90, v91
	global_store_dwordx4 v[114:115], v[82:85], off offset:256
	s_waitcnt vmcnt(14)
	v_lshlrev_b32_e32 v92, 16, v192
	v_and_b32_e32 v93, 0xffff0000, v192
	v_add_u32_e32 v82, 0x80, v146
	v_ashrrev_i32_e32 v83, 31, v82
	v_lshlrev_b64 v[82:83], 11, v[82:83]
	v_lshl_add_u64 v[82:83], v[144:145], 0, v[82:83]
	v_lshlrev_b32_e32 v94, 16, v193
	v_and_b32_e32 v95, 0xffff0000, v193
	v_lshlrev_b32_e32 v96, 16, v194
	v_and_b32_e32 v97, 0xffff0000, v194
	v_lshlrev_b32_e32 v104, 16, v195
	v_and_b32_e32 v105, 0xffff0000, v195
	v_pk_fma_f32 v[78:79], v[92:93], s[20:21], v[78:79] op_sel_hi:[1,0,1]
	v_pk_fma_f32 v[92:93], v[104:105], s[20:21], v[76:77] op_sel_hi:[1,0,1]
	v_pk_fma_f32 v[76:77], v[96:97], s[20:21], v[74:75] op_sel_hi:[1,0,1]
	v_pk_fma_f32 v[80:81], v[94:95], s[20:21], v[80:81] op_sel_hi:[1,0,1]
	v_cvt_pk_bf16_f32 v74, v78, v79
	v_cvt_pk_bf16_f32 v75, v80, v81
	v_cvt_pk_bf16_f32 v76, v76, v77
	s_waitcnt vmcnt(14)
	v_lshlrev_b32_e32 v106, 16, v196
	v_and_b32_e32 v107, 0xffff0000, v196
	v_lshlrev_b32_e32 v108, 16, v198
	v_and_b32_e32 v109, 0xffff0000, v198
	v_lshlrev_b32_e32 v102, 16, v199
	v_and_b32_e32 v103, 0xffff0000, v199
	v_cvt_pk_bf16_f32 v77, v92, v93
	v_pk_fma_f32 v[70:71], v[106:107], s[20:21], v[70:71] op_sel_hi:[1,0,1]
	global_store_dwordx4 v[98:99], v[74:77], off
	v_lshlrev_b32_e32 v100, 16, v197
	v_and_b32_e32 v101, 0xffff0000, v197
	v_pk_fma_f32 v[76:77], v[102:103], s[20:21], v[68:69] op_sel_hi:[1,0,1]
	v_pk_fma_f32 v[72:73], v[100:101], s[20:21], v[72:73] op_sel_hi:[1,0,1]
	v_cvt_pk_bf16_f32 v68, v70, v71
	v_pk_fma_f32 v[66:67], v[108:109], s[20:21], v[66:67] op_sel_hi:[1,0,1]
	v_cvt_pk_bf16_f32 v69, v72, v73
	v_cvt_pk_bf16_f32 v70, v66, v67
	v_bfe_u32 v66, v76, 16, 1
	v_add3_u32 v66, v76, v66, s51
	v_lshrrev_b32_e32 v71, 16, v66
	v_add_u32_e32 v66, 0x90, v146
	v_ashrrev_i32_e32 v67, 31, v66
	v_lshlrev_b64 v[66:67], 11, v[66:67]
	v_lshl_add_u64 v[66:67], v[144:145], 0, v[66:67]
	v_bfe_u32 v76, v77, 16, 1
	v_add3_u32 v76, v77, v76, s51
	v_and_or_b32 v71, v76, s50, v71
	global_store_dwordx4 v[98:99], v[68:71], off offset:256
	s_waitcnt vmcnt(14)
	v_lshlrev_b32_e32 v76, 16, v200
	v_and_b32_e32 v77, 0xffff0000, v200
	v_lshlrev_b32_e32 v78, 16, v201
	v_and_b32_e32 v79, 0xffff0000, v201
	v_lshlrev_b32_e32 v80, 16, v202
	v_and_b32_e32 v81, 0xffff0000, v202
	v_lshlrev_b32_e32 v84, 16, v203
	v_and_b32_e32 v85, 0xffff0000, v203
	v_pk_fma_f32 v[62:63], v[76:77], s[20:21], v[62:63] op_sel_hi:[1,0,1]
	v_pk_fma_f32 v[76:77], v[84:85], s[20:21], v[60:61] op_sel_hi:[1,0,1]
	v_pk_fma_f32 v[60:61], v[80:81], s[20:21], v[58:59] op_sel_hi:[1,0,1]
	v_pk_fma_f32 v[64:65], v[78:79], s[20:21], v[64:65] op_sel_hi:[1,0,1]
	v_cvt_pk_bf16_f32 v58, v62, v63
	v_cvt_pk_bf16_f32 v59, v64, v65
	v_cvt_pk_bf16_f32 v60, v60, v61
	s_waitcnt vmcnt(14)
	v_lshlrev_b32_e32 v86, 16, v204
	v_and_b32_e32 v87, 0xffff0000, v204
	v_lshlrev_b32_e32 v92, 16, v206
	v_and_b32_e32 v93, 0xffff0000, v206
	v_lshlrev_b32_e32 v90, 16, v207
	v_and_b32_e32 v91, 0xffff0000, v207
	v_cvt_pk_bf16_f32 v61, v76, v77
	v_pk_fma_f32 v[54:55], v[86:87], s[20:21], v[54:55] op_sel_hi:[1,0,1]
	global_store_dwordx4 v[82:83], v[58:61], off
	v_lshlrev_b32_e32 v88, 16, v205
	v_and_b32_e32 v89, 0xffff0000, v205
	v_pk_fma_f32 v[58:59], v[90:91], s[20:21], v[52:53] op_sel_hi:[1,0,1]
	v_pk_fma_f32 v[52:53], v[92:93], s[20:21], v[50:51] op_sel_hi:[1,0,1]
	v_pk_fma_f32 v[56:57], v[88:89], s[20:21], v[56:57] op_sel_hi:[1,0,1]
	v_cvt_pk_bf16_f32 v50, v54, v55
	v_cvt_pk_bf16_f32 v51, v56, v57
	v_cvt_pk_bf16_f32 v52, v52, v53
	v_cvt_pk_bf16_f32 v53, v58, v59
	global_store_dwordx4 v[82:83], v[50:53], off offset:256
	s_waitcnt vmcnt(14)
	v_lshlrev_b32_e32 v60, 16, v208
	v_and_b32_e32 v61, 0xffff0000, v208
	v_add_u32_e32 v50, 0xa0, v146
	v_ashrrev_i32_e32 v51, 31, v50
	v_lshlrev_b64 v[50:51], 11, v[50:51]
	v_lshl_add_u64 v[50:51], v[144:145], 0, v[50:51]
	v_lshlrev_b32_e32 v62, 16, v209
	v_and_b32_e32 v63, 0xffff0000, v209
	v_lshlrev_b32_e32 v64, 16, v210
	v_and_b32_e32 v65, 0xffff0000, v210
	v_lshlrev_b32_e32 v72, 16, v211
	v_and_b32_e32 v73, 0xffff0000, v211
	v_pk_fma_f32 v[46:47], v[60:61], s[20:21], v[46:47] op_sel_hi:[1,0,1]
	v_pk_fma_f32 v[60:61], v[72:73], s[20:21], v[44:45] op_sel_hi:[1,0,1]
	v_pk_fma_f32 v[44:45], v[64:65], s[20:21], v[42:43] op_sel_hi:[1,0,1]
	v_pk_fma_f32 v[48:49], v[62:63], s[20:21], v[48:49] op_sel_hi:[1,0,1]
	v_cvt_pk_bf16_f32 v42, v46, v47
	v_cvt_pk_bf16_f32 v43, v48, v49
	v_cvt_pk_bf16_f32 v44, v44, v45
	s_waitcnt vmcnt(14)
	v_lshlrev_b32_e32 v74, 16, v222
	v_and_b32_e32 v75, 0xffff0000, v222
	v_lshlrev_b32_e32 v76, 16, v224
	v_and_b32_e32 v77, 0xffff0000, v224
	v_lshlrev_b32_e32 v70, 16, v225
	v_and_b32_e32 v71, 0xffff0000, v225
	v_cvt_pk_bf16_f32 v45, v60, v61
	v_pk_fma_f32 v[38:39], v[74:75], s[20:21], v[38:39] op_sel_hi:[1,0,1]
	global_store_dwordx4 v[66:67], v[42:45], off
	v_lshlrev_b32_e32 v68, 16, v223
	v_and_b32_e32 v69, 0xffff0000, v223
	v_pk_fma_f32 v[42:43], v[70:71], s[20:21], v[36:37] op_sel_hi:[1,0,1]
	v_pk_fma_f32 v[36:37], v[76:77], s[20:21], v[34:35] op_sel_hi:[1,0,1]
	v_pk_fma_f32 v[40:41], v[68:69], s[20:21], v[40:41] op_sel_hi:[1,0,1]
	v_cvt_pk_bf16_f32 v34, v38, v39
	v_cvt_pk_bf16_f32 v35, v40, v41
	v_bfe_u32 v38, v36, 16, 1
	v_add3_u32 v36, v36, v38, s51
	v_bfe_u32 v38, v37, 16, 1
	v_add3_u32 v37, v37, v38, s51
	v_add_u32_e32 v38, 0xb0, v146
	v_ashrrev_i32_e32 v39, 31, v38
	v_lshlrev_b64 v[38:39], 11, v[38:39]
	v_lshl_add_u64 v[44:45], v[144:145], 0, v[38:39]
	v_lshrrev_b32_e32 v36, 16, v36
	v_and_or_b32 v36, v37, s50, v36
	v_cvt_pk_bf16_f32 v37, v42, v43
	global_store_dwordx4 v[66:67], v[34:37], off offset:256
	s_waitcnt vmcnt(14)
	v_lshlrev_b32_e32 v42, 16, v226
	v_and_b32_e32 v43, 0xffff0000, v226
	v_lshlrev_b32_e32 v46, 16, v227
	v_and_b32_e32 v47, 0xffff0000, v227
	v_lshlrev_b32_e32 v48, 16, v228
	v_and_b32_e32 v49, 0xffff0000, v228
	v_lshlrev_b32_e32 v52, 16, v229
	v_and_b32_e32 v53, 0xffff0000, v229
	v_pk_fma_f32 v[30:31], v[42:43], s[20:21], v[30:31] op_sel_hi:[1,0,1]
	v_pk_fma_f32 v[42:43], v[52:53], s[20:21], v[28:29] op_sel_hi:[1,0,1]
	v_pk_fma_f32 v[28:29], v[48:49], s[20:21], v[26:27] op_sel_hi:[1,0,1]
	v_pk_fma_f32 v[32:33], v[46:47], s[20:21], v[32:33] op_sel_hi:[1,0,1]
	v_cvt_pk_bf16_f32 v26, v30, v31
	v_cvt_pk_bf16_f32 v27, v32, v33
	v_cvt_pk_bf16_f32 v28, v28, v29
	s_waitcnt vmcnt(14)
	v_lshlrev_b32_e32 v54, 16, v230
	v_and_b32_e32 v55, 0xffff0000, v230
	v_lshlrev_b32_e32 v60, 16, v232
	v_and_b32_e32 v61, 0xffff0000, v232
	v_lshlrev_b32_e32 v58, 16, v233
	v_and_b32_e32 v59, 0xffff0000, v233
	v_cvt_pk_bf16_f32 v29, v42, v43
	v_pk_fma_f32 v[22:23], v[54:55], s[20:21], v[22:23] op_sel_hi:[1,0,1]
	global_store_dwordx4 v[50:51], v[26:29], off
	v_lshlrev_b32_e32 v56, 16, v231
	v_and_b32_e32 v57, 0xffff0000, v231
	v_pk_fma_f32 v[26:27], v[58:59], s[20:21], v[20:21] op_sel_hi:[1,0,1]
	v_pk_fma_f32 v[20:21], v[60:61], s[20:21], v[18:19] op_sel_hi:[1,0,1]
	v_pk_fma_f32 v[24:25], v[56:57], s[20:21], v[24:25] op_sel_hi:[1,0,1]
	v_cvt_pk_bf16_f32 v18, v22, v23
	v_cvt_pk_bf16_f32 v19, v24, v25
	v_cvt_pk_bf16_f32 v20, v20, v21
	v_cvt_pk_bf16_f32 v21, v26, v27
	global_store_dwordx4 v[50:51], v[18:21], off offset:256
	s_waitcnt vmcnt(14)
	v_lshlrev_b32_e32 v22, 16, v236
	v_and_b32_e32 v23, 0xffff0000, v236
	v_lshlrev_b32_e32 v18, 16, v234
	v_and_b32_e32 v19, 0xffff0000, v234
	v_lshlrev_b32_e32 v24, 16, v237
	v_and_b32_e32 v25, 0xffff0000, v237
	v_pk_fma_f32 v[14:15], v[18:19], s[20:21], v[14:15] op_sel_hi:[1,0,1]
	v_pk_fma_f32 v[18:19], v[24:25], s[20:21], v[12:13] op_sel_hi:[1,0,1]
	v_pk_fma_f32 v[12:13], v[22:23], s[20:21], v[10:11] op_sel_hi:[1,0,1]
	v_lshlrev_b32_e32 v20, 16, v235
	v_and_b32_e32 v21, 0xffff0000, v235
	v_pk_fma_f32 v[16:17], v[20:21], s[20:21], v[16:17] op_sel_hi:[1,0,1]
	v_cvt_pk_bf16_f32 v10, v14, v15
	v_cvt_pk_bf16_f32 v11, v16, v17
	v_cvt_pk_bf16_f32 v12, v12, v13
	s_waitcnt vmcnt(14)
	v_lshlrev_b32_e32 v26, 16, v238
	v_and_b32_e32 v27, 0xffff0000, v238
	v_lshlrev_b32_e32 v30, 16, v240
	v_and_b32_e32 v31, 0xffff0000, v240
	v_lshlrev_b32_e32 v32, 16, v241
	v_and_b32_e32 v33, 0xffff0000, v241
	v_cvt_pk_bf16_f32 v13, v18, v19
	v_pk_fma_f32 v[6:7], v[26:27], s[20:21], v[6:7] op_sel_hi:[1,0,1]
	global_store_dwordx4 v[44:45], v[10:13], off
	v_lshlrev_b32_e32 v28, 16, v239
	v_and_b32_e32 v29, 0xffff0000, v239
	v_pk_fma_f32 v[10:11], v[32:33], s[20:21], v[4:5] op_sel_hi:[1,0,1]
	v_pk_fma_f32 v[4:5], v[30:31], s[20:21], v[2:3] op_sel_hi:[1,0,1]
	v_pk_fma_f32 v[8:9], v[28:29], s[20:21], v[8:9] op_sel_hi:[1,0,1]
	v_cvt_pk_bf16_f32 v2, v6, v7
	v_cvt_pk_bf16_f32 v3, v8, v9
	v_cvt_pk_bf16_f32 v4, v4, v5
	v_cvt_pk_bf16_f32 v5, v10, v11
	global_store_dwordx4 v[44:45], v[2:5], off offset:256
	s_cbranch_vccnz .LBB0_588
	s_andn2_b64 vcc, exec, s[4:5]
	s_cbranch_vccnz .LBB0_587
	s_barrier
	s_branch .LBB0_587

.LBB0_682:
	s_or_b64 exec, exec, s[0:1]
	s_mov_b32 s1, 0
	s_barrier
	s_add_u32 s9, s94, s1
	s_mov_b32 s6, s21
	v_readlane_b32 s1, v254, 22
	v_mov_b32_e32 v2, v0
	s_addc_u32 s30, s95, 0
	v_bfe_i32 v4, v2, 27, 1
	v_lshlrev_b32_e32 v1, 4, v2
	v_lshrrev_b32_e32 v4, 22, v4
	v_add_u32_e32 v4, v1, v4
	v_and_b32_e32 v4, 0xfffffc00, v4
	v_sub_u32_e32 v1, v1, v4
	v_ashrrev_i32_e32 v3, 31, v2
	v_lshrrev_b32_e32 v4, 4, v1
	v_lshrrev_b32_e32 v3, 26, v3
	v_bitop3_b32 v4, v4, v1, 32 bitop3:0x6c
	v_ashrrev_i32_e32 v1, 31, v1
	v_add_u32_e32 v3, v2, v3
	v_lshrrev_b32_e32 v1, 26, v1
	v_ashrrev_i32_e32 v3, 6, v3
	v_add_u32_e32 v1, v4, v1
	v_lshlrev_b32_e32 v5, 3, v3
	v_ashrrev_i32_e32 v1, 6, v1
	v_and_b32_e32 v5, -16, v5
	v_mul_i32_i24_e32 v6, 64, v1
	v_add_u32_e32 v5, v1, v5
	v_sub_u32_e32 v4, v4, v6
	v_mov_b32_e32 v6, 1
	s_add_u32 s31, s9, 0x19a00000
	v_lshlrev_b32_e32 v3, 5, v3
	v_ashrrev_i16_sdwa v4, v6, sext(v4) dst_sel:DWORD dst_unused:UNUSED_PAD src0_sel:DWORD src1_sel:BYTE_0
	v_lshlrev_b32_e32 v6, 1, v5
	v_lshrrev_b32_e32 v7, 2, v5
	v_and_b32_e32 v1, 3, v1
	s_mov_b32 s3, 0xffffe0
	s_addc_u32 s33, s30, 0
	v_and_b32_e32 v3, 32, v3
	v_bfe_i32 v4, v4, 0, 16
	v_and_b32_e32 v6, 24, v6
	v_and_b32_e32 v7, 4, v7
	v_and_or_b32 v1, v5, s3, v1
	s_add_u32 s34, s9, 0x1c00000
	v_readfirstlane_b32 s2, v2
	v_or3_b32 v1, v1, v7, v6
	v_add_lshl_u32 v4, v3, v4, 1
	s_movk_i32 s3, 0xb00
	s_addc_u32 s35, s30, 0
	v_mad_u64_u32 v[130:131], s[4:5], v5, s3, v[4:5]
	v_mad_u32_u24 v1, v1, s3, v4
	s_ashr_i32 s3, s2, 6
	s_lshl_b32 s4, s3, 10
	s_lshl_b32 s7, s6, 4
	s_lshr_b32 s5, s6, 2
	s_ashr_i32 s6, s6, 4
	s_add_i32 s37, s4, 0
	s_and_b32 s4, s7, 0x70
	s_add_i32 s36, s4, s6
	s_ashr_i32 s1, s2, 8
	s_and_b32 s80, s5, 2
	s_mul_i32 s5, s36, 0xb0000
	s_mul_hi_i32 s4, s36, 0xb0000
	s_add_u32 s22, s31, s5
	s_addc_u32 s23, s33, s4
	s_mul_i32 s4, s80, 0xb0000
	s_add_u32 s24, s34, s4
	s_addc_u32 s25, s35, 0
	s_add_i32 s38, s37, 0x10000
	s_mov_b32 m0, s38
	s_nop 0
	global_load_lds_dwordx4 v1, s[24:25]
	s_add_u32 s4, s24, 0x2c000
	s_addc_u32 s5, s25, 0
	s_add_i32 s39, s37, 0x12000
	s_mov_b32 m0, s39
	s_nop 0
	global_load_lds_dwordx4 v1, s[4:5]
	s_add_u32 s4, s24, 0x58000
	s_addc_u32 s5, s25, 0
	s_add_i32 s42, s37, 0x14000
	s_mov_b32 m0, s42
	s_nop 0
	global_load_lds_dwordx4 v1, s[4:5]
	s_add_u32 s4, s4, 0x2c000
	s_addc_u32 s5, s5, 0
	s_add_i32 s43, s37, 0x16000
	s_mov_b32 m0, s43
	s_nop 0
	global_load_lds_dwordx4 v1, s[4:5]
	s_mov_b32 m0, s37
	s_nop 0
	global_load_lds_dwordx4 v130, s[22:23]
	s_add_u32 s4, s22, 0x2c000
	s_addc_u32 s5, s23, 0
	s_add_i32 s44, s37, 0x2000
	s_mov_b32 m0, s44
	s_nop 0
	global_load_lds_dwordx4 v130, s[4:5]
	s_add_u32 s4, s22, 0x58000
	s_addc_u32 s5, s23, 0
	s_add_i32 s45, s37, 0x4000
	s_mov_b32 m0, s45
	s_nop 0
	global_load_lds_dwordx4 v130, s[4:5]
	s_add_u32 s6, s4, 0x2c000
	s_addc_u32 s7, s5, 0
	s_add_i32 s46, s37, 0x6000
	s_mov_b32 m0, s46
	s_nop 0
	global_load_lds_dwordx4 v130, s[6:7]
	s_cmp_eq_u32 s1, 1
	s_mov_b32 s0, 0
	s_cselect_b64 s[4:5], -1, 0
	s_cmp_lg_u32 s1, 1
	s_cbranch_scc1 .LBB0_684
	s_barrier
.LBB0_684:
	v_and_b32_e32 v3, 15, v2
	v_lshlrev_b32_e32 v4, 1, v2
	v_lshlrev_b32_e32 v5, 5, v2
	v_lshlrev_b32_e32 v2, 2, v2
	s_add_u32 s47, s9, 0xca00000
	v_lshlrev_b32_e32 v3, 6, v3
	v_and_b32_e32 v4, 32, v4
	v_and_b32_e32 v2, 32, v2
	s_addc_u32 s50, s30, 0
	s_and_b32 s3, s3, 3
	v_bitop3_b32 v2, v4, v2, v3 bitop3:0x36
	s_movk_i32 s6, 0x400
	v_and_or_b32 v2, v5, s6, v2
	s_add_u32 s6, s24, 0x80
	s_addc_u32 s7, s25, 0
	s_add_i32 s51, s37, 0x18000
	s_waitcnt vmcnt(2)
	s_barrier
	s_mov_b32 m0, s51
	s_nop 0
	global_load_lds_dwordx4 v1, s[6:7]
	s_add_u32 s6, s6, 0x2c000
	s_addc_u32 s7, s7, 0
	s_add_i32 s52, s37, 0x1a000
	s_mov_b32 m0, s52
	s_nop 0
	global_load_lds_dwordx4 v1, s[6:7]
	s_add_u32 s6, s22, 0x80
	s_addc_u32 s7, s23, 0
	s_add_i32 s53, s37, 0x8000
	s_mov_b32 m0, s53
	s_nop 0
	global_load_lds_dwordx4 v130, s[6:7]
	s_add_u32 s6, s6, 0x2c000
	s_addc_u32 s7, s7, 0
	s_add_i32 s55, s37, 0xa000
	s_mov_b32 m0, s55
	s_nop 0
	global_load_lds_dwordx4 v130, s[6:7]
	s_add_u32 s6, s24, 0x58080
	s_addc_u32 s7, s25, 0
	s_add_i32 s62, s37, 0x1c000
	s_mov_b32 m0, s62
	s_nop 0
	global_load_lds_dwordx4 v1, s[6:7]
	s_add_u32 s6, s6, 0x2c000
	s_addc_u32 s7, s7, 0
	s_add_i32 s63, s37, 0x1e000
	s_mov_b32 m0, s63
	s_nop 0
	global_load_lds_dwordx4 v1, s[6:7]
	v_lshl_or_b32 v3, s1, 13, v2
	v_lshl_or_b32 v2, s3, 12, v2
	s_waitcnt vmcnt(6)
	s_add_i32 s72, s37, 0xc000
	s_add_i32 s73, s37, 0xe000
	s_cmpk_lt_u32 s2, 0x100
	v_add_u32_e32 v2, 0, v2
	s_cselect_b64 s[6:7], -1, 0
	s_lshl_b32 s74, s1, 6
	s_lshl_b32 s75, s3, 5
	s_or_b32 s76, s80, 1
	s_mov_b64 s[26:27], -1
	v_add_u32_e32 v131, 0x10000, v2
	v_add_u32_e32 v140, 0x14000, v2
	v_add_u32_e32 v141, 0, v3
	v_mov_b32_e32 v142, 0x7a7a7a7a
	v_add_u32_e32 v143, 0x18000, v2
	v_add_u32_e32 v144, 0x1c000, v2
	v_mov_b32_e32 v133, 0
	s_mov_b32 s77, 0xffff0000
	s_mov_b32 s8, 0x3fb504f3
	s_movk_i32 s79, 0x7fff
	s_barrier
	s_branch .LBB0_687

.LBB0_696:
	ds_read_b128 v[146:149], v131
	ds_read_b128 v[150:153], v131 offset:16
	ds_read_b128 v[158:161], v131 offset:2064
	ds_read_b128 v[154:157], v131 offset:2048
	ds_read_b128 v[162:165], v140
	ds_read_b128 v[166:169], v140 offset:16
	ds_read_b128 v[174:177], v140 offset:2064
	ds_read_b128 v[170:173], v140 offset:2048
	s_add_u32 s24, s22, 0xfffa8080
	s_addc_u32 s25, s23, -1
	s_cmp_eq_u32 s82, 18
	s_cselect_b32 s28, s10, s24
	s_cselect_b32 s29, s11, s25
	s_cselect_b32 s26, s20, s1
	s_cselect_b32 s27, s21, s81
	s_add_u32 s24, s28, 0x80
	s_addc_u32 s25, s29, 0
	ds_read_b128 v[178:181], v141
	ds_read_b128 v[182:185], v141 offset:16
	ds_read_b128 v[190:193], v141 offset:2064
	ds_read_b128 v[186:189], v141 offset:2048
	ds_read_b128 v[198:201], v141 offset:4112
	ds_read_b128 v[194:197], v141 offset:4096
	ds_read_b128 v[206:209], v141 offset:6160
	ds_read_b128 v[202:205], v141 offset:6144
	s_mov_b32 m0, s72
	s_nop 0
	global_load_lds_dwordx4 v130, s[22:23]
	s_add_u32 s84, s22, 0x2c000
	s_addc_u32 s85, s23, 0
	s_mov_b32 m0, s73
	s_nop 0
	global_load_lds_dwordx4 v130, s[84:85]
	s_waitcnt vmcnt(8)
	s_waitcnt lgkmcnt(0)
	s_barrier
	s_setprio 1
	s_waitcnt lgkmcnt(6)
	v_mfma_scale_f32_16x16x128_f8f6f4 v[126:129], v[146:153], v[178:185], v[126:129], v142, v142 op_sel_hi:[0,0,0]
	v_mfma_scale_f32_16x16x128_f8f6f4 v[122:125], v[154:161], v[178:185], v[122:125], v142, v142 op_sel_hi:[0,0,0]
	s_waitcnt lgkmcnt(4)
	v_mfma_scale_f32_16x16x128_f8f6f4 v[110:113], v[146:153], v[186:193], v[110:113], v142, v142 op_sel_hi:[0,0,0]
	v_mfma_scale_f32_16x16x128_f8f6f4 v[106:109], v[154:161], v[186:193], v[106:109], v142, v142 op_sel_hi:[0,0,0]
	s_waitcnt lgkmcnt(2)
	v_mfma_scale_f32_16x16x128_f8f6f4 v[134:137], v[146:153], v[194:201], v[94:97], v142, v142 op_sel_hi:[0,0,0]
	v_mfma_scale_f32_16x16x128_f8f6f4 v[210:213], v[154:161], v[194:201], v[90:93], v142, v142 op_sel_hi:[0,0,0]
	s_waitcnt lgkmcnt(0)
	v_mfma_scale_f32_16x16x128_f8f6f4 v[214:217], v[146:153], v[202:209], v[78:81], v142, v142 op_sel_hi:[0,0,0]
	v_mfma_scale_f32_16x16x128_f8f6f4 v[218:221], v[154:161], v[202:209], v[74:77], v142, v142 op_sel_hi:[0,0,0]
	s_setprio 0
	s_setprio 1
	v_mfma_scale_f32_16x16x128_f8f6f4 v[118:121], v[162:169], v[178:185], v[118:121], v142, v142 op_sel_hi:[0,0,0]
	v_mfma_scale_f32_16x16x128_f8f6f4 v[114:117], v[170:177], v[178:185], v[114:117], v142, v142 op_sel_hi:[0,0,0]
	v_mfma_scale_f32_16x16x128_f8f6f4 v[102:105], v[162:169], v[186:193], v[102:105], v142, v142 op_sel_hi:[0,0,0]
	v_mfma_scale_f32_16x16x128_f8f6f4 v[98:101], v[170:177], v[186:193], v[98:101], v142, v142 op_sel_hi:[0,0,0]
	v_mfma_scale_f32_16x16x128_f8f6f4 v[178:181], v[162:169], v[194:201], v[86:89], v142, v142 op_sel_hi:[0,0,0]
	v_mfma_scale_f32_16x16x128_f8f6f4 v[182:185], v[170:177], v[194:201], v[82:85], v142, v142 op_sel_hi:[0,0,0]
	v_mfma_scale_f32_16x16x128_f8f6f4 v[186:189], v[162:169], v[202:209], v[70:73], v142, v142 op_sel_hi:[0,0,0]
	v_mfma_scale_f32_16x16x128_f8f6f4 v[190:193], v[170:177], v[202:209], v[66:69], v142, v142 op_sel_hi:[0,0,0]
	s_setprio 0
	s_barrier
	s_add_u32 s84, s26, 0x2c000
	s_nop 3
	ds_read_b128 v[66:69], v141 offset:16384
	ds_read_b128 v[70:73], v141 offset:16400
	ds_read_b128 v[78:81], v141 offset:18448
	ds_read_b128 v[74:77], v141 offset:18432
	ds_read_b128 v[86:89], v141 offset:20496
	ds_read_b128 v[82:85], v141 offset:20480
	ds_read_b128 v[94:97], v141 offset:22544
	ds_read_b128 v[90:93], v141 offset:22528
	s_mov_b32 m0, s38
	s_nop 0
	global_load_lds_dwordx4 v1, s[26:27]
	s_addc_u32 s85, s27, 0
	s_mov_b32 m0, s39
	s_nop 0
	global_load_lds_dwordx4 v1, s[84:85]
	s_add_u32 s84, s26, 0x58000
	s_addc_u32 s85, s27, 0
	s_mov_b32 m0, s42
	s_nop 0
	global_load_lds_dwordx4 v1, s[84:85]
	s_add_u32 s84, s84, 0x2c000
	s_addc_u32 s85, s85, 0
	s_mov_b32 m0, s43
	s_nop 0
	global_load_lds_dwordx4 v1, s[84:85]
	s_add_u32 s84, s28, 0x2c000
	s_mov_b32 m0, s37
	s_nop 0
	global_load_lds_dwordx4 v130, s[28:29]
	s_addc_u32 s85, s29, 0
	s_mov_b32 m0, s44
	s_nop 0
	global_load_lds_dwordx4 v130, s[84:85]
	s_waitcnt vmcnt(8)
	s_waitcnt lgkmcnt(0)
	s_barrier
	s_setprio 1
	s_waitcnt lgkmcnt(6)
	v_mfma_scale_f32_16x16x128_f8f6f4 v[62:65], v[146:153], v[66:73], v[62:65], v142, v142 op_sel_hi:[0,0,0]
	v_mfma_scale_f32_16x16x128_f8f6f4 v[58:61], v[154:161], v[66:73], v[58:61], v142, v142 op_sel_hi:[0,0,0]
	s_waitcnt lgkmcnt(4)
	v_mfma_scale_f32_16x16x128_f8f6f4 v[194:197], v[146:153], v[74:81], v[46:49], v142, v142 op_sel_hi:[0,0,0]
	v_mfma_scale_f32_16x16x128_f8f6f4 v[198:201], v[154:161], v[74:81], v[42:45], v142, v142 op_sel_hi:[0,0,0]
	s_waitcnt lgkmcnt(2)
	v_mfma_scale_f32_16x16x128_f8f6f4 v[202:205], v[146:153], v[82:89], v[30:33], v142, v142 op_sel_hi:[0,0,0]
	v_mfma_scale_f32_16x16x128_f8f6f4 v[206:209], v[154:161], v[82:89], v[26:29], v142, v142 op_sel_hi:[0,0,0]
	s_waitcnt lgkmcnt(0)
	v_mfma_scale_f32_16x16x128_f8f6f4 v[222:225], v[146:153], v[90:97], v[14:17], v142, v142 op_sel_hi:[0,0,0]
	v_mfma_scale_f32_16x16x128_f8f6f4 v[226:229], v[154:161], v[90:97], v[10:13], v142, v142 op_sel_hi:[0,0,0]
	s_setprio 0
	s_setprio 1
	v_mfma_scale_f32_16x16x128_f8f6f4 v[54:57], v[162:169], v[66:73], v[54:57], v142, v142 op_sel_hi:[0,0,0]
	v_mfma_scale_f32_16x16x128_f8f6f4 v[50:53], v[170:177], v[66:73], v[50:53], v142, v142 op_sel_hi:[0,0,0]
	v_mfma_scale_f32_16x16x128_f8f6f4 v[230:233], v[162:169], v[74:81], v[38:41], v142, v142 op_sel_hi:[0,0,0]
	v_mfma_scale_f32_16x16x128_f8f6f4 v[234:237], v[170:177], v[74:81], v[34:37], v142, v142 op_sel_hi:[0,0,0]
	v_mfma_scale_f32_16x16x128_f8f6f4 v[238:241], v[162:169], v[82:89], v[22:25], v142, v142 op_sel_hi:[0,0,0]
	v_mfma_scale_f32_16x16x128_f8f6f4 v[242:245], v[170:177], v[82:89], v[18:21], v142, v142 op_sel_hi:[0,0,0]
	v_mfma_scale_f32_16x16x128_f8f6f4 v[246:249], v[162:169], v[90:97], v[6:9], v142, v142 op_sel_hi:[0,0,0]
	v_mfma_scale_f32_16x16x128_f8f6f4 v[250:253], v[170:177], v[90:97], v[2:5], v142, v142 op_sel_hi:[0,0,0]
	s_setprio 0
	s_barrier
	s_nop 4
	ds_read_b128 v[2:5], v143
	ds_read_b128 v[6:9], v143 offset:16
	ds_read_b128 v[22:25], v143 offset:2064
	ds_read_b128 v[18:21], v143 offset:2048
	ds_read_b128 v[146:149], v144
	ds_read_b128 v[150:153], v144 offset:16
	ds_read_b128 v[158:161], v144 offset:2064
	ds_read_b128 v[154:157], v144 offset:2048
	ds_read_b128 v[10:13], v141 offset:32768
	ds_read_b128 v[14:17], v141 offset:32784
	ds_read_b128 v[30:33], v141 offset:34832
	ds_read_b128 v[26:29], v141 offset:34816
	ds_read_b128 v[38:41], v141 offset:36880
	ds_read_b128 v[34:37], v141 offset:36864
	ds_read_b128 v[46:49], v141 offset:38928
	ds_read_b128 v[42:45], v141 offset:38912
	s_add_u32 s28, s28, 0x58000
	s_addc_u32 s29, s29, 0
	s_mov_b32 m0, s45
	s_nop 0
	global_load_lds_dwordx4 v130, s[28:29]
	s_add_u32 s28, s28, 0x2c000
	s_addc_u32 s29, s29, 0
	s_mov_b32 m0, s46
	s_nop 0
	global_load_lds_dwordx4 v130, s[28:29]
	s_waitcnt vmcnt(8)
	s_waitcnt lgkmcnt(0)
	s_barrier
	s_setprio 1
	s_waitcnt lgkmcnt(6)
	v_mfma_scale_f32_16x16x128_f8f6f4 v[126:129], v[2:9], v[10:17], v[126:129], v142, v142 op_sel_hi:[0,0,0]
	v_mfma_scale_f32_16x16x128_f8f6f4 v[122:125], v[18:25], v[10:17], v[122:125], v142, v142 op_sel_hi:[0,0,0]
	s_waitcnt lgkmcnt(4)
	v_mfma_scale_f32_16x16x128_f8f6f4 v[110:113], v[2:9], v[26:33], v[110:113], v142, v142 op_sel_hi:[0,0,0]
	v_mfma_scale_f32_16x16x128_f8f6f4 v[106:109], v[18:25], v[26:33], v[106:109], v142, v142 op_sel_hi:[0,0,0]
	s_waitcnt lgkmcnt(2)
	v_mfma_scale_f32_16x16x128_f8f6f4 v[94:97], v[2:9], v[34:41], v[134:137], v142, v142 op_sel_hi:[0,0,0]
	v_mfma_scale_f32_16x16x128_f8f6f4 v[90:93], v[18:25], v[34:41], v[210:213], v142, v142 op_sel_hi:[0,0,0]
	s_waitcnt lgkmcnt(0)
	v_mfma_scale_f32_16x16x128_f8f6f4 v[78:81], v[2:9], v[42:49], v[214:217], v142, v142 op_sel_hi:[0,0,0]
	v_mfma_scale_f32_16x16x128_f8f6f4 v[74:77], v[18:25], v[42:49], v[218:221], v142, v142 op_sel_hi:[0,0,0]
	s_setprio 0
	s_setprio 1
	v_mfma_scale_f32_16x16x128_f8f6f4 v[118:121], v[146:153], v[10:17], v[118:121], v142, v142 op_sel_hi:[0,0,0]
	v_mfma_scale_f32_16x16x128_f8f6f4 v[114:117], v[154:161], v[10:17], v[114:117], v142, v142 op_sel_hi:[0,0,0]
	v_mfma_scale_f32_16x16x128_f8f6f4 v[102:105], v[146:153], v[26:33], v[102:105], v142, v142 op_sel_hi:[0,0,0]
	v_mfma_scale_f32_16x16x128_f8f6f4 v[98:101], v[154:161], v[26:33], v[98:101], v142, v142 op_sel_hi:[0,0,0]
	v_mfma_scale_f32_16x16x128_f8f6f4 v[86:89], v[146:153], v[34:41], v[178:181], v142, v142 op_sel_hi:[0,0,0]
	v_mfma_scale_f32_16x16x128_f8f6f4 v[82:85], v[154:161], v[34:41], v[182:185], v142, v142 op_sel_hi:[0,0,0]
	v_mfma_scale_f32_16x16x128_f8f6f4 v[70:73], v[146:153], v[42:49], v[186:189], v142, v142 op_sel_hi:[0,0,0]
	v_mfma_scale_f32_16x16x128_f8f6f4 v[66:69], v[154:161], v[42:49], v[190:193], v142, v142 op_sel_hi:[0,0,0]
	s_setprio 0
	s_barrier
	s_add_u32 s28, s26, 0x80
	s_addc_u32 s29, s27, 0
	ds_read_b128 v[34:37], v141 offset:49152
	ds_read_b128 v[38:41], v141 offset:49168
	ds_read_b128 v[166:169], v141 offset:51216
	ds_read_b128 v[162:165], v141 offset:51200
	ds_read_b128 v[174:177], v141 offset:53264
	ds_read_b128 v[170:173], v141 offset:53248
	ds_read_b128 v[182:185], v141 offset:55312
	ds_read_b128 v[178:181], v141 offset:55296
	s_mov_b32 m0, s51
	s_nop 0
	global_load_lds_dwordx4 v1, s[28:29]
	s_add_u32 s28, s28, 0x2c000
	s_addc_u32 s29, s29, 0
	s_add_u32 s26, s26, 0x58080
	s_mov_b32 m0, s52
	s_nop 0
	global_load_lds_dwordx4 v1, s[28:29]
	s_addc_u32 s27, s27, 0
	s_mov_b32 m0, s62
	s_nop 0
	global_load_lds_dwordx4 v1, s[26:27]
	s_add_u32 s26, s26, 0x2c000
	s_addc_u32 s27, s27, 0
	s_mov_b32 m0, s63
	s_nop 0
	global_load_lds_dwordx4 v1, s[26:27]
	s_mov_b32 m0, s53
	s_nop 0
	global_load_lds_dwordx4 v130, s[24:25]
	s_add_u32 s24, s24, 0x2c000
	s_addc_u32 s25, s25, 0
	s_mov_b32 m0, s55
	s_nop 0
	global_load_lds_dwordx4 v130, s[24:25]
	s_waitcnt vmcnt(8)
	s_waitcnt lgkmcnt(0)
	s_barrier
	s_setprio 1
	s_waitcnt lgkmcnt(6)
	v_mfma_scale_f32_16x16x128_f8f6f4 v[62:65], v[2:9], v[34:41], v[62:65], v142, v142 op_sel_hi:[0,0,0]
	v_mfma_scale_f32_16x16x128_f8f6f4 v[58:61], v[18:25], v[34:41], v[58:61], v142, v142 op_sel_hi:[0,0,0]
	s_waitcnt lgkmcnt(4)
	v_mfma_scale_f32_16x16x128_f8f6f4 v[46:49], v[2:9], v[162:169], v[194:197], v142, v142 op_sel_hi:[0,0,0]
	v_mfma_scale_f32_16x16x128_f8f6f4 v[42:45], v[18:25], v[162:169], v[198:201], v142, v142 op_sel_hi:[0,0,0]
	s_waitcnt lgkmcnt(2)
	v_mfma_scale_f32_16x16x128_f8f6f4 v[30:33], v[2:9], v[170:177], v[202:205], v142, v142 op_sel_hi:[0,0,0]
	v_mfma_scale_f32_16x16x128_f8f6f4 v[26:29], v[18:25], v[170:177], v[206:209], v142, v142 op_sel_hi:[0,0,0]
	s_waitcnt lgkmcnt(0)
	v_mfma_scale_f32_16x16x128_f8f6f4 v[14:17], v[2:9], v[178:185], v[222:225], v142, v142 op_sel_hi:[0,0,0]
	v_mfma_scale_f32_16x16x128_f8f6f4 v[10:13], v[18:25], v[178:185], v[226:229], v142, v142 op_sel_hi:[0,0,0]
	s_setprio 0
	s_setprio 1
	v_mfma_scale_f32_16x16x128_f8f6f4 v[54:57], v[146:153], v[34:41], v[54:57], v142, v142 op_sel_hi:[0,0,0]
	v_mfma_scale_f32_16x16x128_f8f6f4 v[50:53], v[154:161], v[34:41], v[50:53], v142, v142 op_sel_hi:[0,0,0]
	v_mfma_scale_f32_16x16x128_f8f6f4 v[38:41], v[146:153], v[162:169], v[230:233], v142, v142 op_sel_hi:[0,0,0]
	v_mfma_scale_f32_16x16x128_f8f6f4 v[34:37], v[154:161], v[162:169], v[234:237], v142, v142 op_sel_hi:[0,0,0]
	v_mfma_scale_f32_16x16x128_f8f6f4 v[22:25], v[146:153], v[170:177], v[238:241], v142, v142 op_sel_hi:[0,0,0]
	v_mfma_scale_f32_16x16x128_f8f6f4 v[18:21], v[154:161], v[170:177], v[242:245], v142, v142 op_sel_hi:[0,0,0]
	v_mfma_scale_f32_16x16x128_f8f6f4 v[6:9], v[146:153], v[178:185], v[246:249], v142, v142 op_sel_hi:[0,0,0]
	v_mfma_scale_f32_16x16x128_f8f6f4 v[2:5], v[154:161], v[178:185], v[250:253], v142, v142 op_sel_hi:[0,0,0]
	s_setprio 0
	s_barrier
	s_add_i32 s82, s82, 2
	s_add_u32 s1, s1, 0x100
	s_addc_u32 s81, s81, 0
	s_add_u32 s22, s22, 0x100
	s_addc_u32 s23, s23, 0
	s_cmp_gt_u32 s82, 19
	s_cbranch_scc0 .LBB0_696
	s_and_b64 vcc, exec, s[6:7]
	s_cbranch_vccz .LBB0_699
	s_barrier

.LBB0_963:
	s_waitcnt vmcnt(0)
	v_lshl_add_u64 v[18:19], v[48:49], 0, s[24:25]
	v_readlane_b32 s72, v254, 4
	v_readlane_b32 s80, v254, 12
	v_readlane_b32 s81, v254, 13
	v_mov_b32_e32 v31, v8
	v_mov_b32_e32 v8, v7
	s_nop 0
	v_mov_b32_e32 v30, v6
	v_mov_b32_e32 v6, v2
	v_mov_b32_e32 v7, v4
	v_mov_b32_e32 v4, v3
	v_mov_b32_e32 v2, v14
	v_mov_b32_e32 v3, v16
	v_mov_b32_e32 v16, v15
	v_mov_b32_e32 v14, v10
	v_mov_b32_e32 v15, v12
	v_mov_b32_e32 v12, v11
	s_add_u32 s24, s24, 0x80
	s_addc_u32 s25, s25, 0
	s_cmpk_eq_i32 s24, 0x200
	v_readlane_b32 s73, v254, 5
	v_readlane_b32 s74, v254, 6
	v_readlane_b32 s75, v254, 7
	v_readlane_b32 s76, v254, 8
	v_readlane_b32 s77, v254, 9
	v_readlane_b32 s78, v254, 10
	v_readlane_b32 s79, v254, 11
	v_readlane_b32 s82, v254, 14
	v_readlane_b32 s83, v254, 15
	v_readlane_b32 s84, v254, 16
	v_readlane_b32 s85, v254, 17
	v_readlane_b32 s86, v254, 18
	v_readlane_b32 s87, v254, 19
	s_waitcnt vmcnt(4)
	v_lshlrev_b32_e32 v11, 16, v89
	v_lshlrev_b32_e32 v10, 16, v88
	v_and_b32_e32 v89, 0xffff0000, v89
	v_and_b32_e32 v88, 0xffff0000, v88
	s_waitcnt vmcnt(3)
	v_pk_add_f32 v[8:9], v[96:97], v[8:9] op_sel_hi:[0,1]
	v_pk_add_f32 v[30:31], v[96:97], v[30:31] op_sel_hi:[0,1]
	s_waitcnt vmcnt(2)
	v_lshlrev_b32_e32 v33, 16, v91
	v_lshlrev_b32_e32 v32, 16, v90
	v_and_b32_e32 v91, 0xffff0000, v91
	v_and_b32_e32 v90, 0xffff0000, v90
	v_pk_add_f32 v[4:5], v[96:97], v[4:5] op_sel_hi:[0,1]
	s_waitcnt vmcnt(1)
	v_lshlrev_b32_e32 v35, 16, v93
	v_lshlrev_b32_e32 v34, 16, v92
	v_pk_add_f32 v[2:3], v[96:97], v[2:3] op_sel_hi:[0,1]
	v_and_b32_e32 v93, 0xffff0000, v93
	v_and_b32_e32 v92, 0xffff0000, v92
	v_pk_add_f32 v[16:17], v[96:97], v[16:17] op_sel_hi:[0,1]
	v_pk_mul_f32 v[8:9], v[8:9], v[88:89]
	v_pk_add_f32 v[6:7], v[96:97], v[6:7] op_sel_hi:[0,1]
	v_pk_add_f32 v[14:15], v[96:97], v[14:15] op_sel_hi:[0,1]
	v_pk_mul_f32 v[10:11], v[30:31], v[10:11]
	v_pk_mul_f32 v[4:5], v[4:5], v[90:91]
	v_pk_mul_f32 v[2:3], v[2:3], v[34:35]
	v_pk_mul_f32 v[16:17], v[16:17], v[92:93]
	v_and_b32_sdwa v97, v9, v60 dst_sel:DWORD dst_unused:UNUSED_PAD src0_sel:WORD_1 src1_sel:DWORD
	v_and_b32_sdwa v90, v8, v60 dst_sel:DWORD dst_unused:UNUSED_PAD src0_sel:WORD_1 src1_sel:DWORD
	v_pk_mul_f32 v[6:7], v[6:7], v[32:33]
	v_and_b32_sdwa v88, v11, v60 dst_sel:DWORD dst_unused:UNUSED_PAD src0_sel:WORD_1 src1_sel:DWORD
	v_and_b32_sdwa v89, v10, v60 dst_sel:DWORD dst_unused:UNUSED_PAD src0_sel:WORD_1 src1_sel:DWORD
	v_and_b32_sdwa v93, v5, v60 dst_sel:DWORD dst_unused:UNUSED_PAD src0_sel:WORD_1 src1_sel:DWORD
	v_and_b32_sdwa v30, v4, v60 dst_sel:DWORD dst_unused:UNUSED_PAD src0_sel:WORD_1 src1_sel:DWORD
	v_and_b32_sdwa v31, v3, v60 dst_sel:DWORD dst_unused:UNUSED_PAD src0_sel:WORD_1 src1_sel:DWORD
	v_and_b32_sdwa v32, v2, v60 dst_sel:DWORD dst_unused:UNUSED_PAD src0_sel:WORD_1 src1_sel:DWORD
	v_and_b32_sdwa v33, v17, v60 dst_sel:DWORD dst_unused:UNUSED_PAD src0_sel:WORD_1 src1_sel:DWORD
	v_and_b32_sdwa v34, v16, v60 dst_sel:DWORD dst_unused:UNUSED_PAD src0_sel:WORD_1 src1_sel:DWORD
	v_add3_u32 v9, v9, v97, s30
	v_add3_u32 v8, v8, v90, s30
	v_and_b32_sdwa v91, v7, v60 dst_sel:DWORD dst_unused:UNUSED_PAD src0_sel:WORD_1 src1_sel:DWORD
	v_and_b32_sdwa v92, v6, v60 dst_sel:DWORD dst_unused:UNUSED_PAD src0_sel:WORD_1 src1_sel:DWORD
	v_add3_u32 v10, v10, v89, s30
	v_add3_u32 v11, v11, v88, s30
	v_add3_u32 v5, v5, v93, s30
	v_add3_u32 v4, v4, v30, s30
	v_add3_u32 v88, v2, v32, s30
	v_add3_u32 v89, v3, v31, s30
	v_add3_u32 v2, v17, v33, s30
	v_add3_u32 v3, v16, v34, s30
	v_and_b32_e32 v9, 0xffff0000, v9
	v_and_b32_e32 v8, 0xffff0000, v8
	v_add3_u32 v6, v6, v92, s30
	v_add3_u32 v7, v7, v91, s30
	v_and_b32_e32 v5, 0xffff0000, v5
	v_and_b32_e32 v4, 0xffff0000, v4
	v_and_b32_e32 v16, 0xffff0000, v2
	v_and_b32_e32 v17, 0xffff0000, v3
	v_or_b32_sdwa v3, v9, v11 dst_sel:DWORD dst_unused:UNUSED_PAD src0_sel:DWORD src1_sel:WORD_1
	v_or_b32_sdwa v2, v8, v10 dst_sel:DWORD dst_unused:UNUSED_PAD src0_sel:DWORD src1_sel:WORD_1
	s_waitcnt vmcnt(0)
	v_lshlrev_b32_e32 v37, 16, v95
	v_lshlrev_b32_e32 v36, 16, v94
	v_and_b32_e32 v95, 0xffff0000, v95
	v_and_b32_e32 v94, 0xffff0000, v94
	v_or_b32_sdwa v5, v5, v7 dst_sel:DWORD dst_unused:UNUSED_PAD src0_sel:DWORD src1_sel:WORD_1
	v_or_b32_sdwa v4, v4, v6 dst_sel:DWORD dst_unused:UNUSED_PAD src0_sel:DWORD src1_sel:WORD_1
	v_or_b32_sdwa v7, v16, v89 dst_sel:DWORD dst_unused:UNUSED_PAD src0_sel:DWORD src1_sel:WORD_1
	v_or_b32_sdwa v6, v17, v88 dst_sel:DWORD dst_unused:UNUSED_PAD src0_sel:DWORD src1_sel:WORD_1
	global_store_dwordx2 v[18:19], v[2:3], off offset:-64
	global_store_dwordx2 v[18:19], v[4:5], off offset:-32
	global_store_dwordx2 v[18:19], v[6:7], off
	v_pk_add_f32 v[2:3], v[96:97], v[12:13] op_sel_hi:[0,1]
	v_pk_mul_f32 v[2:3], v[2:3], v[94:95]
	v_pk_mul_f32 v[14:15], v[14:15], v[36:37]
	v_and_b32_sdwa v6, v3, v60 dst_sel:DWORD dst_unused:UNUSED_PAD src0_sel:WORD_1 src1_sel:DWORD
	v_and_b32_sdwa v7, v2, v60 dst_sel:DWORD dst_unused:UNUSED_PAD src0_sel:WORD_1 src1_sel:DWORD
	v_and_b32_sdwa v4, v15, v60 dst_sel:DWORD dst_unused:UNUSED_PAD src0_sel:WORD_1 src1_sel:DWORD
	v_and_b32_sdwa v5, v14, v60 dst_sel:DWORD dst_unused:UNUSED_PAD src0_sel:WORD_1 src1_sel:DWORD
	v_add3_u32 v3, v3, v6, s30
	v_add3_u32 v2, v2, v7, s30
	v_add3_u32 v5, v14, v5, s30
	v_add3_u32 v4, v15, v4, s30
	v_and_b32_e32 v3, 0xffff0000, v3
	v_and_b32_e32 v2, 0xffff0000, v2
	v_or_b32_sdwa v3, v3, v4 dst_sel:DWORD dst_unused:UNUSED_PAD src0_sel:DWORD src1_sel:WORD_1
	v_or_b32_sdwa v2, v2, v5 dst_sel:DWORD dst_unused:UNUSED_PAD src0_sel:DWORD src1_sel:WORD_1
	global_store_dwordx2 v[18:19], v[2:3], off offset:32
	s_cbranch_scc1 .LBB0_981
.LBB0_964:
	v_lshl_add_u64 v[6:7], v[46:47], 0, s[24:25]
	v_add_co_u32_e32 v2, vcc, 0x10a00000, v6
	s_nop 1
	v_addc_co_u32_e32 v3, vcc, 0, v7, vcc
	s_barrier
	global_load_dwordx4 v[2:5], v[2:3], off offset:512
	v_lshl_add_u64 v[6:7], v[6:7], 0, s[26:27]
	global_load_dwordx4 v[6:9], v[6:7], off offset:16
	v_add_u32_e32 v50, s24, v44
	v_ashrrev_i32_e32 v51, 31, v50
	v_lshl_add_u64 v[98:99], v[48:49], 0, s[24:25]
	v_readlane_b32 s100, v254, 12
	v_readlane_b32 s101, v254, 13
	global_load_dwordx2 v[88:89], v[98:99], off offset:-64
	global_load_dwordx2 v[90:91], v[98:99], off offset:-32
	global_load_dwordx2 v[92:93], v[98:99], off
	global_load_dwordx2 v[94:95], v[98:99], off offset:32
	v_lshl_add_u64 v[96:97], v[50:51], 2, s[100:101]
	global_load_dword v96, v[96:97], off offset:2048
	s_waitcnt vmcnt(6)
	v_lshlrev_b32_e32 v10, 16, v2
	v_and_b32_e32 v2, 0xffff0000, v2
	v_add_f32_e32 v18, 0, v10
	v_lshlrev_b32_e32 v11, 16, v3
	v_add_f32_e32 v18, v18, v2
	v_and_b32_e32 v3, 0xffff0000, v3
	v_add_f32_e32 v18, v18, v11
	v_lshlrev_b32_e32 v12, 16, v4
	v_add_f32_e32 v18, v18, v3
	v_and_b32_e32 v4, 0xffff0000, v4
	v_add_f32_e32 v18, v18, v12
	v_lshlrev_b32_e32 v13, 16, v5
	v_add_f32_e32 v18, v18, v4
	v_and_b32_e32 v5, 0xffff0000, v5
	v_add_f32_e32 v18, v18, v13
	s_waitcnt vmcnt(5)
	v_lshlrev_b32_e32 v14, 16, v6
	v_add_f32_e32 v18, v18, v5
	v_and_b32_e32 v6, 0xffff0000, v6
	v_add_f32_e32 v18, v18, v14
	v_lshlrev_b32_e32 v15, 16, v7
	v_add_f32_e32 v18, v18, v6
	v_and_b32_e32 v7, 0xffff0000, v7
	v_add_f32_e32 v18, v18, v15
	v_lshlrev_b32_e32 v16, 16, v8
	v_add_f32_e32 v18, v18, v7
	v_and_b32_e32 v8, 0xffff0000, v8
	v_add_f32_e32 v18, v18, v16
	v_lshlrev_b32_e32 v17, 16, v9
	v_add_f32_e32 v18, v18, v8
	v_and_b32_e32 v9, 0xffff0000, v9
	v_add_f32_e32 v18, v18, v17
	v_add_f32_e32 v18, v18, v9
	s_waitcnt lgkmcnt(0)
	s_nop 1
	v_add_f32_dpp v18, v18, v18 quad_perm:[1,0,3,2] row_mask:0xf bank_mask:0xf
	s_nop 1
	v_add_f32_dpp v18, v18, v18 quad_perm:[2,3,0,1] row_mask:0xf bank_mask:0xf
	v_fmac_f32_e32 v2, 0xbc800000, v18
	v_fmac_f32_e32 v10, 0xbc800000, v18
	v_fmac_f32_e32 v11, 0xbc800000, v18
	v_fmac_f32_e32 v3, 0xbc800000, v18
	v_fmac_f32_e32 v12, 0xbc800000, v18
	v_fmac_f32_e32 v4, 0xbc800000, v18
	v_fmac_f32_e32 v13, 0xbc800000, v18
	v_fmac_f32_e32 v5, 0xbc800000, v18
	v_fmac_f32_e32 v14, 0xbc800000, v18
	v_fmac_f32_e32 v6, 0xbc800000, v18
	v_fmac_f32_e32 v15, 0xbc800000, v18
	v_fmac_f32_e32 v7, 0xbc800000, v18
	v_fmac_f32_e32 v16, 0xbc800000, v18
	v_fmac_f32_e32 v8, 0xbc800000, v18
	v_fmac_f32_e32 v17, 0xbc800000, v18
	v_fmac_f32_e32 v9, 0xbc800000, v18
	v_mul_f32_e32 v18, v2, v2
	v_fmac_f32_e32 v18, v10, v10
	v_fmac_f32_e32 v18, v11, v11
	v_fmac_f32_e32 v18, v3, v3
	v_fmac_f32_e32 v18, v12, v12
	v_fmac_f32_e32 v18, v4, v4
	v_fmac_f32_e32 v18, v13, v13
	v_fmac_f32_e32 v18, v5, v5
	v_fmac_f32_e32 v18, v14, v14
	v_fmac_f32_e32 v18, v6, v6
	v_fmac_f32_e32 v18, v15, v15
	v_fmac_f32_e32 v18, v7, v7
	v_fmac_f32_e32 v18, v16, v16
	v_fmac_f32_e32 v18, v8, v8
	v_fmac_f32_e32 v18, v17, v17
	v_fmac_f32_e32 v18, v9, v9
	s_waitcnt lgkmcnt(0)
	s_nop 1
	v_add_f32_dpp v18, v18, v18 quad_perm:[1,0,3,2] row_mask:0xf bank_mask:0xf
	s_nop 1
	v_add_f32_dpp v18, v18, v18 quad_perm:[2,3,0,1] row_mask:0xf bank_mask:0xf
	v_fmamk_f32 v18, v18, 0x3c800000, v39
	v_mul_f32_e32 v19, 0x4f800000, v18
	v_cmp_gt_f32_e32 vcc, s28, v18
	s_nop 1
	v_cndmask_b32_e32 v18, v18, v19, vcc
	v_sqrt_f32_e32 v19, v18
	s_nop 0
	v_add_u32_e32 v20, -1, v19
	v_add_u32_e32 v21, 1, v19
	v_fma_f32 v22, -v20, v19, v18
	v_fma_f32 v23, -v21, v19, v18
	v_cmp_ge_f32_e64 s[0:1], 0, v22
	s_nop 1
	v_cndmask_b32_e64 v19, v19, v20, s[0:1]
	v_cmp_lt_f32_e64 s[0:1], 0, v23
	s_nop 1
	v_cndmask_b32_e64 v19, v19, v21, s[0:1]
	v_mul_f32_e32 v20, 0x37800000, v19
	v_cndmask_b32_e32 v19, v19, v20, vcc
	v_cmp_class_f32_e32 vcc, v18, v54
	s_nop 1
	v_cndmask_b32_e32 v18, v19, v18, vcc
	v_div_scale_f32 v19, s[0:1], v18, v18, 1.0
	v_rcp_f32_e32 v20, v19
	v_div_scale_f32 v21, vcc, 1.0, v18, 1.0
	v_fma_f32 v22, -v19, v20, 1.0
	v_fmac_f32_e32 v20, v22, v20
	v_mul_f32_e32 v22, v21, v20
	v_fma_f32 v23, -v19, v22, v21
	v_fmac_f32_e32 v22, v23, v20
	v_fma_f32 v19, -v19, v22, v21
	v_div_fmas_f32 v19, v19, v20, v22
	v_div_fixup_f32 v18, v19, v18, 1.0
	v_mul_f32_e32 v10, v10, v18
	v_mul_f32_e32 v2, v2, v18
	v_mul_f32_e32 v11, v11, v18
	v_mul_f32_e32 v3, v3, v18
	v_mul_f32_e32 v12, v12, v18
	v_mul_f32_e32 v4, v4, v18
	v_mul_f32_e32 v13, v13, v18
	v_mul_f32_e32 v5, v5, v18
	v_mul_f32_e32 v14, v14, v18
	v_mul_f32_e32 v6, v6, v18
	v_mul_f32_e32 v15, v15, v18
	v_mul_f32_e32 v7, v7, v18
	v_mul_f32_e32 v16, v16, v18
	v_mul_f32_e32 v8, v8, v18
	v_bfe_u32 v19, v10, 16, 1
	v_bfe_u32 v20, v2, 16, 1
	v_mul_f32_e32 v17, v17, v18
	v_bfe_u32 v21, v11, 16, 1
	v_bfe_u32 v22, v3, 16, 1
	v_bfe_u32 v23, v12, 16, 1
	v_bfe_u32 v24, v4, 16, 1
	v_bfe_u32 v25, v13, 16, 1
	v_bfe_u32 v26, v5, 16, 1
	v_bfe_u32 v27, v14, 16, 1
	v_bfe_u32 v28, v6, 16, 1
	v_bfe_u32 v29, v15, 16, 1
	v_bfe_u32 v30, v7, 16, 1
	v_bfe_u32 v31, v16, 16, 1
	v_bfe_u32 v32, v8, 16, 1
	v_add3_u32 v10, v10, v19, s30
	v_add3_u32 v2, v2, v20, s30
	v_add3_u32 v11, v11, v21, s30
	v_add3_u32 v3, v3, v22, s30
	v_add3_u32 v12, v12, v23, s30
	v_add3_u32 v4, v4, v24, s30
	v_add3_u32 v13, v13, v25, s30
	v_add3_u32 v5, v5, v26, s30
	v_add3_u32 v14, v14, v27, s30
	v_add3_u32 v6, v6, v28, s30
	v_add3_u32 v15, v15, v29, s30
	v_add3_u32 v7, v7, v30, s30
	v_add3_u32 v16, v16, v31, s30
	v_add3_u32 v8, v8, v32, s30
	ds_write_b16_d16_hi v56, v10
	ds_write_b16_d16_hi v56, v2 offset:272
	ds_write_b16_d16_hi v56, v11 offset:544
	ds_write_b16_d16_hi v56, v3 offset:816
	ds_write_b16_d16_hi v56, v12 offset:1088
	ds_write_b16_d16_hi v56, v4 offset:1360
	ds_write_b16_d16_hi v56, v13 offset:1632
	ds_write_b16_d16_hi v56, v5 offset:1904
	ds_write_b16_d16_hi v56, v14 offset:2176
	ds_write_b16_d16_hi v56, v6 offset:2448
	ds_write_b16_d16_hi v56, v15 offset:2720
	ds_write_b16_d16_hi v56, v7 offset:2992
	ds_write_b16_d16_hi v56, v16 offset:3264
	ds_write_b16_d16_hi v56, v8 offset:3536
	v_bfe_u32 v2, v17, 16, 1
	v_add3_u32 v2, v17, v2, s30
	ds_write_b16_d16_hi v56, v2 offset:3808
	v_mul_f32_e32 v2, v9, v18
	v_bfe_u32 v3, v2, 16, 1
	v_add3_u32 v2, v2, v3, s30
	ds_write_b16_d16_hi v56, v2 offset:4080
	v_lshlrev_b64 v[2:3], 8, v[50:51]
	s_and_b64 vcc, exec, s[2:3]
	v_lshl_add_u64 v[2:3], v[42:43], 0, v[2:3]
	s_cbranch_vccnz .LBB0_969
	global_load_dwordx4 v[30:33], v[2:3], off
	v_cndmask_b32_e64 v4, 0, 1, s[16:17]
	v_cmp_ne_u32_e64 s[8:9], 1, v4
	s_andn2_b64 vcc, exec, s[16:17]
	s_cbranch_vccz .LBB0_970

.LBB0_1208:
	v_lshl_add_u32 v146, s29, 8, v152
	s_lshl_b32 s18, s43, 8
	s_ashr_i32 s19, s18, 31
	v_ashrrev_i32_e32 v147, 31, v146
	v_lshl_add_u64 v[144:145], s[18:19], 1, v[138:139]
	v_lshlrev_b64 v[148:149], 11, v[146:147]
	v_lshl_add_u64 v[150:151], v[144:145], 0, v[148:149]
	global_load_dwordx4 v[156:159], v[150:151], off
	global_load_dwordx4 v[160:163], v[150:151], off offset:256
	v_or_b32_e32 v148, 16, v146
	v_ashrrev_i32_e32 v149, 31, v148
	v_lshlrev_b64 v[148:149], 11, v[148:149]
	v_lshl_add_u64 v[148:149], v[144:145], 0, v[148:149]
	global_load_dwordx4 v[164:167], v[148:149], off
	global_load_dwordx4 v[168:171], v[148:149], off offset:256
	v_or_b32_e32 v242, 32, v146
	v_ashrrev_i32_e32 v243, 31, v242
	v_lshlrev_b64 v[242:243], 11, v[242:243]
	v_lshl_add_u64 v[242:243], v[144:145], 0, v[242:243]
	global_load_dwordx4 v[184:187], v[242:243], off
	global_load_dwordx4 v[188:191], v[242:243], off offset:256
	v_or_b32_e32 v244, 48, v146
	v_ashrrev_i32_e32 v245, 31, v244
	v_lshlrev_b64 v[244:245], 11, v[244:245]
	v_lshl_add_u64 v[244:245], v[144:145], 0, v[244:245]
	global_load_dwordx4 v[192:195], v[244:245], off
	global_load_dwordx4 v[196:199], v[244:245], off offset:256
	v_add_u32_e32 v246, 0x80, v146
	v_ashrrev_i32_e32 v247, 31, v246
	v_lshlrev_b64 v[246:247], 11, v[246:247]
	v_lshl_add_u64 v[246:247], v[144:145], 0, v[246:247]
	global_load_dwordx4 v[200:203], v[246:247], off
	global_load_dwordx4 v[204:207], v[246:247], off offset:256
	v_add_u32_e32 v248, 0x90, v146
	v_ashrrev_i32_e32 v249, 31, v248
	v_lshlrev_b64 v[248:249], 11, v[248:249]
	v_lshl_add_u64 v[248:249], v[144:145], 0, v[248:249]
	global_load_dwordx4 v[208:211], v[248:249], off
	global_load_dwordx4 v[222:225], v[248:249], off offset:256
	v_add_u32_e32 v250, 0xa0, v146
	v_ashrrev_i32_e32 v251, 31, v250
	v_lshlrev_b64 v[250:251], 11, v[250:251]
	v_lshl_add_u64 v[250:251], v[144:145], 0, v[250:251]
	global_load_dwordx4 v[226:229], v[250:251], off
	global_load_dwordx4 v[230:233], v[250:251], off offset:256
	v_add_u32_e32 v252, 0xb0, v146
	v_ashrrev_i32_e32 v253, 31, v252
	v_lshlrev_b64 v[252:253], 11, v[252:253]
	v_lshl_add_u64 v[252:253], v[144:145], 0, v[252:253]
	global_load_dwordx4 v[234:237], v[252:253], off
	global_load_dwordx4 v[238:241], v[252:253], off offset:256
	v_or_b32_e32 v172, 32, v146
	s_and_b64 vcc, exec, s[2:3]
	s_mov_b64 s[2:3], -1
	s_waitcnt vmcnt(12)
	v_lshlrev_b32_e32 v174, 16, v156
	v_and_b32_e32 v175, 0xffff0000, v156
	v_lshlrev_b32_e32 v156, 16, v157
	v_and_b32_e32 v157, 0xffff0000, v157
	v_lshlrev_b32_e32 v176, 16, v158
	v_and_b32_e32 v177, 0xffff0000, v158
	v_lshlrev_b32_e32 v158, 16, v159
	v_and_b32_e32 v159, 0xffff0000, v159
	v_lshlrev_b32_e32 v178, 16, v160
	v_and_b32_e32 v179, 0xffff0000, v160
	v_lshlrev_b32_e32 v160, 16, v161
	v_and_b32_e32 v161, 0xffff0000, v161
	v_lshlrev_b32_e32 v180, 16, v162
	v_and_b32_e32 v181, 0xffff0000, v162
	v_lshlrev_b32_e32 v162, 16, v163
	v_and_b32_e32 v163, 0xffff0000, v163
	v_pk_fma_f32 v[128:129], v[156:157], s[12:13], v[128:129] op_sel_hi:[1,0,1]
	v_pk_fma_f32 v[126:127], v[174:175], s[12:13], v[126:127] op_sel_hi:[1,0,1]
	v_pk_fma_f32 v[124:125], v[158:159], s[12:13], v[124:125] op_sel_hi:[1,0,1]
	v_pk_fma_f32 v[122:123], v[176:177], s[12:13], v[122:123] op_sel_hi:[1,0,1]
	v_pk_fma_f32 v[120:121], v[160:161], s[12:13], v[120:121] op_sel_hi:[1,0,1]
	v_pk_fma_f32 v[118:119], v[178:179], s[12:13], v[118:119] op_sel_hi:[1,0,1]
	v_pk_fma_f32 v[116:117], v[162:163], s[12:13], v[116:117] op_sel_hi:[1,0,1]
	v_pk_fma_f32 v[114:115], v[180:181], s[12:13], v[114:115] op_sel_hi:[1,0,1]
	v_bfe_u32 v147, v126, 16, 1
	v_bfe_u32 v158, v128, 16, 1
	v_bfe_u32 v157, v127, 16, 1
	v_bfe_u32 v159, v129, 16, 1
	v_bfe_u32 v173, v118, 16, 1
	v_bfe_u32 v175, v120, 16, 1
	v_bfe_u32 v177, v114, 16, 1
	v_bfe_u32 v178, v115, 16, 1
	v_bfe_u32 v179, v116, 16, 1
	v_bfe_u32 v180, v117, 16, 1
	v_add3_u32 v126, v126, v147, s39
	v_add3_u32 v128, v128, v158, s39
	v_bfe_u32 v174, v119, 16, 1
	v_bfe_u32 v176, v121, 16, 1
	v_add3_u32 v127, v127, v157, s39
	v_add3_u32 v129, v129, v159, s39
	v_add3_u32 v118, v118, v173, s39
	v_add3_u32 v120, v120, v175, s39
	v_add3_u32 v114, v114, v177, s39
	v_add3_u32 v147, v115, v178, s39
	v_add3_u32 v115, v116, v179, s39
	v_add3_u32 v157, v117, v180, s39
	v_lshrrev_b32_e32 v116, 16, v126
	v_lshrrev_b32_e32 v117, 16, v128
	v_add3_u32 v119, v119, v174, s39
	v_add3_u32 v121, v121, v176, s39
	v_lshrrev_b32_e32 v118, 16, v118
	v_lshrrev_b32_e32 v120, 16, v120
	v_lshrrev_b32_e32 v126, 16, v114
	v_lshrrev_b32_e32 v128, 16, v115
	v_and_or_b32 v114, v127, s38, v116
	v_and_or_b32 v115, v129, s38, v117
	v_cvt_pk_bf16_f32 v116, v122, v123
	v_cvt_pk_bf16_f32 v117, v124, v125
	v_ashrrev_i32_e32 v173, 31, v172
	v_and_or_b32 v118, v119, s38, v118
	v_and_or_b32 v119, v121, s38, v120
	v_and_or_b32 v120, v147, s38, v126
	v_and_or_b32 v121, v157, s38, v128
	global_store_dwordx4 v[150:151], v[114:117], off
	global_store_dwordx4 v[150:151], v[118:121], off offset:256
	v_lshlrev_b32_e32 v156, 16, v164
	v_lshlrev_b64 v[114:115], 11, v[172:173]
	v_lshl_add_u64 v[114:115], v[144:145], 0, v[114:115]
	v_and_b32_e32 v157, 0xffff0000, v164
	v_lshlrev_b32_e32 v124, 16, v165
	v_and_b32_e32 v125, 0xffff0000, v165
	v_lshlrev_b32_e32 v126, 16, v166
	v_and_b32_e32 v127, 0xffff0000, v166
	v_lshlrev_b32_e32 v128, 16, v167
	v_and_b32_e32 v129, 0xffff0000, v167
	v_pk_fma_f32 v[110:111], v[156:157], s[12:13], v[110:111] op_sel_hi:[1,0,1]
	v_pk_fma_f32 v[112:113], v[124:125], s[12:13], v[112:113] op_sel_hi:[1,0,1]
	v_pk_fma_f32 v[124:125], v[128:129], s[12:13], v[108:109] op_sel_hi:[1,0,1]
	v_pk_fma_f32 v[108:109], v[126:127], s[12:13], v[106:107] op_sel_hi:[1,0,1]
	v_cvt_pk_bf16_f32 v106, v110, v111
	v_cvt_pk_bf16_f32 v107, v112, v113
	v_cvt_pk_bf16_f32 v108, v108, v109
	v_lshlrev_b32_e32 v150, 16, v168
	v_and_b32_e32 v151, 0xffff0000, v168
	v_lshlrev_b32_e32 v162, 16, v171
	v_and_b32_e32 v163, 0xffff0000, v171
	v_cvt_pk_bf16_f32 v109, v124, v125
	v_pk_fma_f32 v[102:103], v[150:151], s[12:13], v[102:103] op_sel_hi:[1,0,1]
	global_store_dwordx4 v[148:149], v[106:109], off
	v_lshlrev_b32_e32 v158, 16, v169
	v_and_b32_e32 v159, 0xffff0000, v169
	v_pk_fma_f32 v[108:109], v[162:163], s[12:13], v[100:101] op_sel_hi:[1,0,1]
	v_pk_fma_f32 v[104:105], v[158:159], s[12:13], v[104:105] op_sel_hi:[1,0,1]
	v_cvt_pk_bf16_f32 v100, v102, v103
	v_lshlrev_b32_e32 v160, 16, v170
	v_and_b32_e32 v161, 0xffff0000, v170
	v_pk_fma_f32 v[98:99], v[160:161], s[12:13], v[98:99] op_sel_hi:[1,0,1]
	v_cvt_pk_bf16_f32 v101, v104, v105
	v_cvt_pk_bf16_f32 v102, v98, v99
	v_bfe_u32 v98, v108, 16, 1
	v_add3_u32 v98, v108, v98, s39
	v_lshrrev_b32_e32 v103, 16, v98
	v_or_b32_e32 v98, 48, v146
	v_ashrrev_i32_e32 v99, 31, v98
	v_lshlrev_b64 v[98:99], 11, v[98:99]
	v_lshl_add_u64 v[98:99], v[144:145], 0, v[98:99]
	v_bfe_u32 v108, v109, 16, 1
	v_add3_u32 v108, v109, v108, s39
	v_and_or_b32 v103, v108, s38, v103
	global_store_dwordx4 v[148:149], v[100:103], off offset:256
	s_waitcnt vmcnt(14)
	v_lshlrev_b32_e32 v108, 16, v184
	v_and_b32_e32 v109, 0xffff0000, v184
	v_lshlrev_b32_e32 v110, 16, v185
	v_and_b32_e32 v111, 0xffff0000, v185
	v_lshlrev_b32_e32 v112, 16, v186
	v_and_b32_e32 v113, 0xffff0000, v186
	v_lshlrev_b32_e32 v116, 16, v187
	v_and_b32_e32 v117, 0xffff0000, v187
	v_pk_fma_f32 v[94:95], v[108:109], s[12:13], v[94:95] op_sel_hi:[1,0,1]
	v_pk_fma_f32 v[108:109], v[116:117], s[12:13], v[92:93] op_sel_hi:[1,0,1]
	v_pk_fma_f32 v[92:93], v[112:113], s[12:13], v[90:91] op_sel_hi:[1,0,1]
	v_pk_fma_f32 v[96:97], v[110:111], s[12:13], v[96:97] op_sel_hi:[1,0,1]
	v_cvt_pk_bf16_f32 v90, v94, v95
	v_cvt_pk_bf16_f32 v91, v96, v97
	v_cvt_pk_bf16_f32 v92, v92, v93
	s_waitcnt vmcnt(14)
	v_lshlrev_b32_e32 v118, 16, v188
	v_and_b32_e32 v119, 0xffff0000, v188
	v_lshlrev_b32_e32 v124, 16, v190
	v_and_b32_e32 v125, 0xffff0000, v190
	v_lshlrev_b32_e32 v122, 16, v191
	v_and_b32_e32 v123, 0xffff0000, v191
	v_cvt_pk_bf16_f32 v93, v108, v109
	v_pk_fma_f32 v[86:87], v[118:119], s[12:13], v[86:87] op_sel_hi:[1,0,1]
	global_store_dwordx4 v[114:115], v[90:93], off
	v_lshlrev_b32_e32 v120, 16, v189
	v_and_b32_e32 v121, 0xffff0000, v189
	v_pk_fma_f32 v[90:91], v[122:123], s[12:13], v[84:85] op_sel_hi:[1,0,1]
	v_pk_fma_f32 v[84:85], v[124:125], s[12:13], v[82:83] op_sel_hi:[1,0,1]
	v_pk_fma_f32 v[88:89], v[120:121], s[12:13], v[88:89] op_sel_hi:[1,0,1]
	v_cvt_pk_bf16_f32 v82, v86, v87
	v_cvt_pk_bf16_f32 v83, v88, v89
	v_cvt_pk_bf16_f32 v84, v84, v85
	v_cvt_pk_bf16_f32 v85, v90, v91
	global_store_dwordx4 v[114:115], v[82:85], off offset:256
	s_waitcnt vmcnt(14)
	v_lshlrev_b32_e32 v92, 16, v192
	v_and_b32_e32 v93, 0xffff0000, v192
	v_add_u32_e32 v82, 0x80, v146
	v_ashrrev_i32_e32 v83, 31, v82
	v_lshlrev_b64 v[82:83], 11, v[82:83]
	v_lshl_add_u64 v[82:83], v[144:145], 0, v[82:83]
	v_lshlrev_b32_e32 v94, 16, v193
	v_and_b32_e32 v95, 0xffff0000, v193
	v_lshlrev_b32_e32 v96, 16, v194
	v_and_b32_e32 v97, 0xffff0000, v194
	v_lshlrev_b32_e32 v104, 16, v195
	v_and_b32_e32 v105, 0xffff0000, v195
	v_pk_fma_f32 v[78:79], v[92:93], s[12:13], v[78:79] op_sel_hi:[1,0,1]
	v_pk_fma_f32 v[92:93], v[104:105], s[12:13], v[76:77] op_sel_hi:[1,0,1]
	v_pk_fma_f32 v[76:77], v[96:97], s[12:13], v[74:75] op_sel_hi:[1,0,1]
	v_pk_fma_f32 v[80:81], v[94:95], s[12:13], v[80:81] op_sel_hi:[1,0,1]
	v_cvt_pk_bf16_f32 v74, v78, v79
	v_cvt_pk_bf16_f32 v75, v80, v81
	v_cvt_pk_bf16_f32 v76, v76, v77
	s_waitcnt vmcnt(14)
	v_lshlrev_b32_e32 v106, 16, v196
	v_and_b32_e32 v107, 0xffff0000, v196
	v_lshlrev_b32_e32 v108, 16, v198
	v_and_b32_e32 v109, 0xffff0000, v198
	v_lshlrev_b32_e32 v102, 16, v199
	v_and_b32_e32 v103, 0xffff0000, v199
	v_cvt_pk_bf16_f32 v77, v92, v93
	v_pk_fma_f32 v[70:71], v[106:107], s[12:13], v[70:71] op_sel_hi:[1,0,1]
	global_store_dwordx4 v[98:99], v[74:77], off
	v_lshlrev_b32_e32 v100, 16, v197
	v_and_b32_e32 v101, 0xffff0000, v197
	v_pk_fma_f32 v[76:77], v[102:103], s[12:13], v[68:69] op_sel_hi:[1,0,1]
	v_pk_fma_f32 v[72:73], v[100:101], s[12:13], v[72:73] op_sel_hi:[1,0,1]
	v_cvt_pk_bf16_f32 v68, v70, v71
	v_pk_fma_f32 v[66:67], v[108:109], s[12:13], v[66:67] op_sel_hi:[1,0,1]
	v_cvt_pk_bf16_f32 v69, v72, v73
	v_cvt_pk_bf16_f32 v70, v66, v67
	v_bfe_u32 v66, v76, 16, 1
	v_add3_u32 v66, v76, v66, s39
	v_lshrrev_b32_e32 v71, 16, v66
	v_add_u32_e32 v66, 0x90, v146
	v_ashrrev_i32_e32 v67, 31, v66
	v_lshlrev_b64 v[66:67], 11, v[66:67]
	v_lshl_add_u64 v[66:67], v[144:145], 0, v[66:67]
	v_bfe_u32 v76, v77, 16, 1
	v_add3_u32 v76, v77, v76, s39
	v_and_or_b32 v71, v76, s38, v71
	global_store_dwordx4 v[98:99], v[68:71], off offset:256
	s_waitcnt vmcnt(14)
	v_lshlrev_b32_e32 v76, 16, v200
	v_and_b32_e32 v77, 0xffff0000, v200
	v_lshlrev_b32_e32 v78, 16, v201
	v_and_b32_e32 v79, 0xffff0000, v201
	v_lshlrev_b32_e32 v80, 16, v202
	v_and_b32_e32 v81, 0xffff0000, v202
	v_lshlrev_b32_e32 v84, 16, v203
	v_and_b32_e32 v85, 0xffff0000, v203
	v_pk_fma_f32 v[62:63], v[76:77], s[12:13], v[62:63] op_sel_hi:[1,0,1]
	v_pk_fma_f32 v[76:77], v[84:85], s[12:13], v[60:61] op_sel_hi:[1,0,1]
	v_pk_fma_f32 v[60:61], v[80:81], s[12:13], v[58:59] op_sel_hi:[1,0,1]
	v_pk_fma_f32 v[64:65], v[78:79], s[12:13], v[64:65] op_sel_hi:[1,0,1]
	v_cvt_pk_bf16_f32 v58, v62, v63
	v_cvt_pk_bf16_f32 v59, v64, v65
	v_cvt_pk_bf16_f32 v60, v60, v61
	s_waitcnt vmcnt(14)
	v_lshlrev_b32_e32 v86, 16, v204
	v_and_b32_e32 v87, 0xffff0000, v204
	v_lshlrev_b32_e32 v92, 16, v206
	v_and_b32_e32 v93, 0xffff0000, v206
	v_lshlrev_b32_e32 v90, 16, v207
	v_and_b32_e32 v91, 0xffff0000, v207
	v_cvt_pk_bf16_f32 v61, v76, v77
	v_pk_fma_f32 v[54:55], v[86:87], s[12:13], v[54:55] op_sel_hi:[1,0,1]
	global_store_dwordx4 v[82:83], v[58:61], off
	v_lshlrev_b32_e32 v88, 16, v205
	v_and_b32_e32 v89, 0xffff0000, v205
	v_pk_fma_f32 v[58:59], v[90:91], s[12:13], v[52:53] op_sel_hi:[1,0,1]
	v_pk_fma_f32 v[52:53], v[92:93], s[12:13], v[50:51] op_sel_hi:[1,0,1]
	v_pk_fma_f32 v[56:57], v[88:89], s[12:13], v[56:57] op_sel_hi:[1,0,1]
	v_cvt_pk_bf16_f32 v50, v54, v55
	v_cvt_pk_bf16_f32 v51, v56, v57
	v_cvt_pk_bf16_f32 v52, v52, v53
	v_cvt_pk_bf16_f32 v53, v58, v59
	global_store_dwordx4 v[82:83], v[50:53], off offset:256
	s_waitcnt vmcnt(14)
	v_lshlrev_b32_e32 v60, 16, v208
	v_and_b32_e32 v61, 0xffff0000, v208
	v_add_u32_e32 v50, 0xa0, v146
	v_ashrrev_i32_e32 v51, 31, v50
	v_lshlrev_b64 v[50:51], 11, v[50:51]
	v_lshl_add_u64 v[50:51], v[144:145], 0, v[50:51]
	v_lshlrev_b32_e32 v62, 16, v209
	v_and_b32_e32 v63, 0xffff0000, v209
	v_lshlrev_b32_e32 v64, 16, v210
	v_and_b32_e32 v65, 0xffff0000, v210
	v_lshlrev_b32_e32 v72, 16, v211
	v_and_b32_e32 v73, 0xffff0000, v211
	v_pk_fma_f32 v[46:47], v[60:61], s[12:13], v[46:47] op_sel_hi:[1,0,1]
	v_pk_fma_f32 v[60:61], v[72:73], s[12:13], v[44:45] op_sel_hi:[1,0,1]
	v_pk_fma_f32 v[44:45], v[64:65], s[12:13], v[42:43] op_sel_hi:[1,0,1]
	v_pk_fma_f32 v[48:49], v[62:63], s[12:13], v[48:49] op_sel_hi:[1,0,1]
	v_cvt_pk_bf16_f32 v42, v46, v47
	v_cvt_pk_bf16_f32 v43, v48, v49
	v_cvt_pk_bf16_f32 v44, v44, v45
	s_waitcnt vmcnt(14)
	v_lshlrev_b32_e32 v74, 16, v222
	v_and_b32_e32 v75, 0xffff0000, v222
	v_lshlrev_b32_e32 v76, 16, v224
	v_and_b32_e32 v77, 0xffff0000, v224
	v_lshlrev_b32_e32 v70, 16, v225
	v_and_b32_e32 v71, 0xffff0000, v225
	v_cvt_pk_bf16_f32 v45, v60, v61
	v_pk_fma_f32 v[38:39], v[74:75], s[12:13], v[38:39] op_sel_hi:[1,0,1]
	global_store_dwordx4 v[66:67], v[42:45], off
	v_lshlrev_b32_e32 v68, 16, v223
	v_and_b32_e32 v69, 0xffff0000, v223
	v_pk_fma_f32 v[42:43], v[70:71], s[12:13], v[36:37] op_sel_hi:[1,0,1]
	v_pk_fma_f32 v[36:37], v[76:77], s[12:13], v[34:35] op_sel_hi:[1,0,1]
	v_pk_fma_f32 v[40:41], v[68:69], s[12:13], v[40:41] op_sel_hi:[1,0,1]
	v_cvt_pk_bf16_f32 v34, v38, v39
	v_cvt_pk_bf16_f32 v35, v40, v41
	v_bfe_u32 v38, v36, 16, 1
	v_add3_u32 v36, v36, v38, s39
	v_bfe_u32 v38, v37, 16, 1
	v_add3_u32 v37, v37, v38, s39
	v_add_u32_e32 v38, 0xb0, v146
	v_ashrrev_i32_e32 v39, 31, v38
	v_lshlrev_b64 v[38:39], 11, v[38:39]
	v_lshl_add_u64 v[44:45], v[144:145], 0, v[38:39]
	v_lshrrev_b32_e32 v36, 16, v36
	v_and_or_b32 v36, v37, s38, v36
	v_cvt_pk_bf16_f32 v37, v42, v43
	global_store_dwordx4 v[66:67], v[34:37], off offset:256
	s_waitcnt vmcnt(14)
	v_lshlrev_b32_e32 v42, 16, v226
	v_and_b32_e32 v43, 0xffff0000, v226
	v_lshlrev_b32_e32 v46, 16, v227
	v_and_b32_e32 v47, 0xffff0000, v227
	v_lshlrev_b32_e32 v48, 16, v228
	v_and_b32_e32 v49, 0xffff0000, v228
	v_lshlrev_b32_e32 v52, 16, v229
	v_and_b32_e32 v53, 0xffff0000, v229
	v_pk_fma_f32 v[30:31], v[42:43], s[12:13], v[30:31] op_sel_hi:[1,0,1]
	v_pk_fma_f32 v[42:43], v[52:53], s[12:13], v[28:29] op_sel_hi:[1,0,1]
	v_pk_fma_f32 v[28:29], v[48:49], s[12:13], v[26:27] op_sel_hi:[1,0,1]
	v_pk_fma_f32 v[32:33], v[46:47], s[12:13], v[32:33] op_sel_hi:[1,0,1]
	v_cvt_pk_bf16_f32 v26, v30, v31
	v_cvt_pk_bf16_f32 v27, v32, v33
	v_cvt_pk_bf16_f32 v28, v28, v29
	s_waitcnt vmcnt(14)
	v_lshlrev_b32_e32 v54, 16, v230
	v_and_b32_e32 v55, 0xffff0000, v230
	v_lshlrev_b32_e32 v60, 16, v232
	v_and_b32_e32 v61, 0xffff0000, v232
	v_lshlrev_b32_e32 v58, 16, v233
	v_and_b32_e32 v59, 0xffff0000, v233
	v_cvt_pk_bf16_f32 v29, v42, v43
	v_pk_fma_f32 v[22:23], v[54:55], s[12:13], v[22:23] op_sel_hi:[1,0,1]
	global_store_dwordx4 v[50:51], v[26:29], off
	v_lshlrev_b32_e32 v56, 16, v231
	v_and_b32_e32 v57, 0xffff0000, v231
	v_pk_fma_f32 v[26:27], v[58:59], s[12:13], v[20:21] op_sel_hi:[1,0,1]
	v_pk_fma_f32 v[20:21], v[60:61], s[12:13], v[18:19] op_sel_hi:[1,0,1]
	v_pk_fma_f32 v[24:25], v[56:57], s[12:13], v[24:25] op_sel_hi:[1,0,1]
	v_cvt_pk_bf16_f32 v18, v22, v23
	v_cvt_pk_bf16_f32 v19, v24, v25
	v_cvt_pk_bf16_f32 v20, v20, v21
	v_cvt_pk_bf16_f32 v21, v26, v27
	global_store_dwordx4 v[50:51], v[18:21], off offset:256
	s_waitcnt vmcnt(14)
	v_lshlrev_b32_e32 v22, 16, v236
	v_and_b32_e32 v23, 0xffff0000, v236
	v_lshlrev_b32_e32 v18, 16, v234
	v_and_b32_e32 v19, 0xffff0000, v234
	v_lshlrev_b32_e32 v24, 16, v237
	v_and_b32_e32 v25, 0xffff0000, v237
	v_pk_fma_f32 v[14:15], v[18:19], s[12:13], v[14:15] op_sel_hi:[1,0,1]
	v_pk_fma_f32 v[18:19], v[24:25], s[12:13], v[12:13] op_sel_hi:[1,0,1]
	v_pk_fma_f32 v[12:13], v[22:23], s[12:13], v[10:11] op_sel_hi:[1,0,1]
	v_lshlrev_b32_e32 v20, 16, v235
	v_and_b32_e32 v21, 0xffff0000, v235
	v_pk_fma_f32 v[16:17], v[20:21], s[12:13], v[16:17] op_sel_hi:[1,0,1]
	v_cvt_pk_bf16_f32 v10, v14, v15
	v_cvt_pk_bf16_f32 v11, v16, v17
	v_cvt_pk_bf16_f32 v12, v12, v13
	s_waitcnt vmcnt(14)
	v_lshlrev_b32_e32 v26, 16, v238
	v_and_b32_e32 v27, 0xffff0000, v238
	v_lshlrev_b32_e32 v30, 16, v240
	v_and_b32_e32 v31, 0xffff0000, v240
	v_lshlrev_b32_e32 v32, 16, v241
	v_and_b32_e32 v33, 0xffff0000, v241
	v_cvt_pk_bf16_f32 v13, v18, v19
	v_pk_fma_f32 v[6:7], v[26:27], s[12:13], v[6:7] op_sel_hi:[1,0,1]
	global_store_dwordx4 v[44:45], v[10:13], off
	v_lshlrev_b32_e32 v28, 16, v239
	v_and_b32_e32 v29, 0xffff0000, v239
	v_pk_fma_f32 v[10:11], v[32:33], s[12:13], v[4:5] op_sel_hi:[1,0,1]
	v_pk_fma_f32 v[4:5], v[30:31], s[12:13], v[2:3] op_sel_hi:[1,0,1]
	v_pk_fma_f32 v[8:9], v[28:29], s[12:13], v[8:9] op_sel_hi:[1,0,1]
	v_cvt_pk_bf16_f32 v2, v6, v7
	v_cvt_pk_bf16_f32 v3, v8, v9
	v_cvt_pk_bf16_f32 v4, v4, v5
	v_cvt_pk_bf16_f32 v5, v10, v11
	global_store_dwordx4 v[44:45], v[2:5], off offset:256
	s_cbranch_vccnz .LBB0_1201
	s_andn2_b64 vcc, exec, s[4:5]
	s_cbranch_vccnz .LBB0_1200
	s_barrier
	s_branch .LBB0_1200

.LBB0_1317:
	v_bfe_i32 v6, v2, 27, 1
	v_lshlrev_b32_e32 v4, 4, v2
	v_lshrrev_b32_e32 v6, 22, v6
	v_add_u32_e32 v6, v4, v6
	v_and_b32_e32 v6, 0xfffffc00, v6
	v_sub_u32_e32 v4, v4, v6
	v_ashrrev_i32_e32 v5, 31, v2
	v_lshrrev_b32_e32 v6, 4, v4
	v_lshrrev_b32_e32 v5, 26, v5
	v_bitop3_b32 v6, v6, v4, 32 bitop3:0x6c
	v_ashrrev_i32_e32 v4, 31, v4
	v_add_u32_e32 v5, v2, v5
	v_lshrrev_b32_e32 v4, 26, v4
	v_ashrrev_i32_e32 v5, 6, v5
	v_add_u32_e32 v4, v6, v4
	s_xor_b64 s[80:81], s[36:37], -1
	v_lshlrev_b32_e32 v7, 3, v5
	v_ashrrev_i32_e32 v4, 6, v4
	s_bitcmp0_b32 s1, 0
	v_readlane_b32 s1, v254, 51
	v_readlane_b32 s4, v254, 53
	v_and_b32_e32 v7, -16, v7
	v_mul_i32_i24_e32 v8, 64, v4
	s_cselect_b32 s1, s1, s4
	v_readlane_b32 s4, v254, 50
	v_readlane_b32 s5, v254, 52
	v_add_u32_e32 v7, v4, v7
	v_sub_u32_e32 v6, v6, v8
	s_cselect_b32 s4, s4, s5
	v_lshlrev_b32_e32 v5, 5, v5
	v_ashrrev_i16_sdwa v6, v201, sext(v6) dst_sel:DWORD dst_unused:UNUSED_PAD src0_sel:DWORD src1_sel:BYTE_0
	v_lshlrev_b32_e32 v8, 1, v7
	v_lshrrev_b32_e32 v9, 2, v7
	v_and_b32_e32 v4, 3, v4
	s_mov_b32 s5, 0x7fffe0
	v_and_b32_e32 v5, 32, v5
	v_bfe_i32 v6, v6, 0, 16
	v_and_b32_e32 v8, 24, v8
	v_and_b32_e32 v9, 4, v9
	v_and_or_b32 v4, v7, s5, v4
	v_or3_b32 v8, v4, v9, v8
	v_add_lshl_u32 v4, v5, v6, 1
	v_mad_u64_u32 v[130:131], s[16:17], v7, s2, v[4:5]
	s_lshl_b32 s5, s26, 10
	s_ashr_i32 s36, s45, 8
	v_mad_u32_u24 v131, v8, s2, v4
	s_add_i32 s5, s5, 0
	s_mul_hi_i32 s15, s14, 0xe0000
	s_mul_i32 s14, s14, 0xe0000
	v_mul_hi_i32 v5, v3, s3
	v_mul_lo_u32 v4, v3, s3
	s_add_u32 s78, s4, s14
	v_lshl_add_u64 v[4:5], s[58:59], 0, v[4:5]
	s_addc_u32 s79, s1, s15
	v_readfirstlane_b32 s92, v4
	s_add_i32 s14, s5, 0x10000
	v_readfirstlane_b32 s93, v5
	s_nop 2
	s_mov_b32 m0, s14
	s_nop 0
	global_load_lds_dwordx4 v131, s[92:93]
	s_add_u32 s16, s92, 0x38000
	s_addc_u32 s17, s93, 0
	s_add_i32 s15, s5, 0x12000
	s_add_u32 s30, s92, 0x70000
	s_mov_b32 m0, s15
	s_nop 0
	global_load_lds_dwordx4 v131, s[16:17]
	s_addc_u32 s31, s93, 0
	s_add_i32 s16, s5, 0x14000
	s_mov_b32 m0, s16
	s_nop 0
	global_load_lds_dwordx4 v131, s[30:31]
	s_add_u32 s30, s30, 0x38000
	s_addc_u32 s31, s31, 0
	s_add_i32 s17, s5, 0x16000
	s_mov_b32 m0, s17
	s_nop 0
	global_load_lds_dwordx4 v131, s[30:31]
	s_add_u32 s30, s78, 0x38000
	s_mov_b32 m0, s5
	s_nop 0
	global_load_lds_dwordx4 v130, s[78:79]
	s_addc_u32 s31, s79, 0
	s_add_i32 s19, s5, 0x2000
	s_mov_b32 m0, s19
	s_nop 0
	global_load_lds_dwordx4 v130, s[30:31]
	s_add_u32 s30, s78, 0x70000
	s_addc_u32 s31, s79, 0
	s_add_i32 s21, s5, 0x4000
	s_mov_b32 m0, s21
	s_nop 0
	global_load_lds_dwordx4 v130, s[30:31]
	s_add_u32 s30, s30, 0x38000
	s_addc_u32 s31, s31, 0
	s_add_i32 s25, s5, 0x6000
	s_mov_b32 m0, s25
	s_nop 0
	global_load_lds_dwordx4 v130, s[30:31]
	s_cmp_eq_u32 s36, 1
	s_cselect_b64 s[82:83], -1, 0
	s_cmp_lg_u32 s36, 1
	s_cbranch_scc1 .LBB0_1319
	s_barrier
.LBB0_1319:
	v_and_b32_e32 v3, 15, v2
	v_lshlrev_b32_e32 v4, 1, v2
	v_lshlrev_b32_e32 v5, 5, v2
	v_lshlrev_b32_e32 v2, 2, v2
	s_and_b32 s37, s26, 3
	v_lshlrev_b32_e32 v3, 6, v3
	v_and_b32_e32 v4, 32, v4
	v_and_b32_e32 v2, 32, v2
	v_bitop3_b32 v2, v4, v2, v3 bitop3:0x36
	s_movk_i32 s26, 0x400
	s_add_u32 s30, s92, 0x80
	v_and_or_b32 v2, v5, s26, v2
	s_addc_u32 s31, s93, 0
	s_add_i32 s26, s5, 0x18000
	s_add_u32 s38, s30, 0x38000
	s_waitcnt vmcnt(2)
	s_barrier
	s_mov_b32 m0, s26
	s_nop 0
	global_load_lds_dwordx4 v131, s[30:31]
	s_addc_u32 s39, s31, 0
	s_add_i32 s30, s5, 0x1a000
	s_mov_b32 m0, s30
	s_nop 0
	global_load_lds_dwordx4 v131, s[38:39]
	s_add_u32 s38, s78, 0x80
	s_addc_u32 s39, s79, 0
	s_add_i32 s31, s5, 0x8000
	s_mov_b32 m0, s31
	s_nop 0
	global_load_lds_dwordx4 v130, s[38:39]
	s_add_u32 s38, s38, 0x38000
	s_addc_u32 s39, s39, 0
	s_add_i32 s33, s5, 0xa000
	s_mov_b32 m0, s33
	s_nop 0
	global_load_lds_dwordx4 v130, s[38:39]
	s_add_u32 s38, s92, 0x70080
	s_addc_u32 s39, s93, 0
	s_add_i32 s34, s5, 0x1c000
	s_mov_b32 m0, s34
	s_nop 0
	global_load_lds_dwordx4 v131, s[38:39]
	s_add_u32 s38, s38, 0x38000
	s_addc_u32 s39, s39, 0
	s_add_i32 s42, s5, 0x1e000
	s_add_i32 s43, s5, 0xc000
	s_add_i32 s44, s5, 0xe000
	s_cmpk_lt_u32 s45, 0x100
	s_cselect_b64 s[84:85], -1, 0
	s_lshl_b32 s45, s36, 6
	s_lshl_b32 s47, s37, 5
	s_lshl_b32 s86, s46, 2
	s_add_i32 s48, s0, s18
	s_cmp_ge_i32 s48, s7
	v_lshl_or_b32 v3, s36, 13, v2
	v_lshl_or_b32 v2, s37, 12, v2
	s_cselect_b64 s[36:37], -1, 0
	s_cmp_ge_i32 s48, s8
	v_cndmask_b32_e64 v4, 0, 1, s[36:37]
	s_cselect_b64 s[36:37], -1, 0
	s_cmp_ge_i32 s48, s9
	v_cndmask_b32_e64 v5, 0, 1, s[36:37]
	s_cselect_b64 vcc, -1, 0
	s_cmp_ge_i32 s48, s10
	v_addc_co_u32_e32 v4, vcc, v4, v5, vcc
	s_cselect_b64 s[36:37], -1, 0
	s_cmp_ge_i32 s48, s11
	v_cndmask_b32_e64 v5, 0, 1, s[36:37]
	s_cselect_b64 vcc, -1, 0
	s_cmp_ge_i32 s48, s12
	v_addc_co_u32_e32 v4, vcc, v4, v5, vcc
	s_cselect_b64 s[36:37], -1, 0
	s_cmp_ge_i32 s48, s13
	s_mov_b32 m0, s42
	s_nop 0
	global_load_lds_dwordx4 v131, s[38:39]
	v_cndmask_b32_e64 v5, 0, 1, s[36:37]
	s_cselect_b64 vcc, -1, 0
	s_waitcnt vmcnt(6)
	v_addc_co_u32_e32 v4, vcc, v4, v5, vcc
	v_lshlrev_b32_e32 v4, 2, v4
	v_readlane_b32 s36, v254, 4
	s_mov_b32 s76, s46
	s_mov_b32 s87, s50
	v_or_b32_e32 v136, s36, v4
	s_mov_b32 s49, 0
	v_add_u32_e32 v137, 0, v2
	v_add_u32_e32 v138, 0, v3
	s_barrier
	s_branch .LBB0_1322

.LBB0_1339:
	v_add_u32_e32 v132, 0x10000, v137
	ds_read_b128 v[140:143], v132
	ds_read_b128 v[144:147], v132 offset:16
	ds_read_b128 v[152:155], v132 offset:2064
	ds_read_b128 v[148:151], v132 offset:2048
	v_add_u32_e32 v132, 0x14000, v137
	ds_read_b128 v[156:159], v132
	ds_read_b128 v[160:163], v132 offset:16
	ds_read_b128 v[168:171], v132 offset:2064
	ds_read_b128 v[164:167], v132 offset:2048
	s_add_u32 s41, s92, 0xfff90080
	s_addc_u32 s46, s93, -1
	s_cmp_eq_u32 s40, 24
	s_cselect_b32 s96, s88, s41
	s_cselect_b32 s97, s89, s46
	s_cselect_b32 s94, s90, s38
	s_cselect_b32 s95, s91, s39
	s_add_u32 s78, s96, 0x80
	s_addc_u32 s79, s97, 0
	ds_read_b128 v[172:175], v138
	ds_read_b128 v[176:179], v138 offset:16
	ds_read_b128 v[184:187], v138 offset:2064
	ds_read_b128 v[180:183], v138 offset:2048
	ds_read_b128 v[210:213], v138 offset:4112
	ds_read_b128 v[206:209], v138 offset:4096
	ds_read_b128 v[218:221], v138 offset:6160
	ds_read_b128 v[214:217], v138 offset:6144
	s_mov_b32 m0, s43
	s_nop 0
	global_load_lds_dwordx4 v130, s[92:93]
	s_add_u32 s72, s92, 0x38000
	s_addc_u32 s73, s93, 0
	s_mov_b32 m0, s44
	s_nop 0
	global_load_lds_dwordx4 v130, s[72:73]
	s_waitcnt vmcnt(8)
	s_waitcnt lgkmcnt(0)
	s_barrier
	s_setprio 1
	s_waitcnt lgkmcnt(6)
	v_mfma_scale_f32_16x16x128_f8f6f4 v[126:129], v[140:147], v[172:179], v[126:129], v200, v200 op_sel_hi:[0,0,0]
	v_mfma_scale_f32_16x16x128_f8f6f4 v[122:125], v[148:155], v[172:179], v[122:125], v200, v200 op_sel_hi:[0,0,0]
	s_waitcnt lgkmcnt(4)
	v_mfma_scale_f32_16x16x128_f8f6f4 v[114:117], v[140:147], v[180:187], v[114:117], v200, v200 op_sel_hi:[0,0,0]
	v_mfma_scale_f32_16x16x128_f8f6f4 v[106:109], v[148:155], v[180:187], v[106:109], v200, v200 op_sel_hi:[0,0,0]
	s_waitcnt lgkmcnt(2)
	v_mfma_scale_f32_16x16x128_f8f6f4 v[98:101], v[140:147], v[206:213], v[98:101], v200, v200 op_sel_hi:[0,0,0]
	v_mfma_scale_f32_16x16x128_f8f6f4 v[132:135], v[148:155], v[206:213], v[90:93], v200, v200 op_sel_hi:[0,0,0]
	s_waitcnt lgkmcnt(0)
	v_mfma_scale_f32_16x16x128_f8f6f4 v[188:191], v[140:147], v[214:221], v[82:85], v200, v200 op_sel_hi:[0,0,0]
	v_mfma_scale_f32_16x16x128_f8f6f4 v[196:199], v[148:155], v[214:221], v[74:77], v200, v200 op_sel_hi:[0,0,0]
	s_setprio 0
	s_setprio 1
	v_mfma_scale_f32_16x16x128_f8f6f4 v[118:121], v[156:163], v[172:179], v[118:121], v200, v200 op_sel_hi:[0,0,0]
	v_mfma_scale_f32_16x16x128_f8f6f4 v[110:113], v[164:171], v[172:179], v[110:113], v200, v200 op_sel_hi:[0,0,0]
	v_mfma_scale_f32_16x16x128_f8f6f4 v[102:105], v[156:163], v[180:187], v[102:105], v200, v200 op_sel_hi:[0,0,0]
	v_mfma_scale_f32_16x16x128_f8f6f4 v[172:175], v[164:171], v[180:187], v[94:97], v200, v200 op_sel_hi:[0,0,0]
	v_mfma_scale_f32_16x16x128_f8f6f4 v[176:179], v[156:163], v[206:213], v[86:89], v200, v200 op_sel_hi:[0,0,0]
	v_mfma_scale_f32_16x16x128_f8f6f4 v[180:183], v[164:171], v[206:213], v[78:81], v200, v200 op_sel_hi:[0,0,0]
	v_mfma_scale_f32_16x16x128_f8f6f4 v[184:187], v[156:163], v[214:221], v[70:73], v200, v200 op_sel_hi:[0,0,0]
	v_mfma_scale_f32_16x16x128_f8f6f4 v[206:209], v[164:171], v[214:221], v[66:69], v200, v200 op_sel_hi:[0,0,0]
	s_setprio 0
	s_barrier
	s_add_u32 s72, s94, 0x38000
	s_nop 3
	ds_read_b128 v[66:69], v138 offset:16384
	ds_read_b128 v[70:73], v138 offset:16400
	ds_read_b128 v[78:81], v138 offset:18448
	ds_read_b128 v[74:77], v138 offset:18432
	ds_read_b128 v[86:89], v138 offset:20496
	ds_read_b128 v[82:85], v138 offset:20480
	ds_read_b128 v[94:97], v138 offset:22544
	ds_read_b128 v[90:93], v138 offset:22528
	s_mov_b32 m0, s14
	s_nop 0
	global_load_lds_dwordx4 v131, s[94:95]
	s_addc_u32 s73, s95, 0
	s_mov_b32 m0, s15
	s_nop 0
	global_load_lds_dwordx4 v131, s[72:73]
	s_add_u32 s72, s94, 0x70000
	s_addc_u32 s73, s95, 0
	s_mov_b32 m0, s16
	s_nop 0
	global_load_lds_dwordx4 v131, s[72:73]
	s_add_u32 s72, s72, 0x38000
	s_addc_u32 s73, s73, 0
	s_mov_b32 m0, s17
	s_nop 0
	global_load_lds_dwordx4 v131, s[72:73]
	s_add_u32 s72, s96, 0x38000
	s_mov_b32 m0, s5
	s_nop 0
	global_load_lds_dwordx4 v130, s[96:97]
	s_addc_u32 s73, s97, 0
	s_mov_b32 m0, s19
	s_nop 0
	global_load_lds_dwordx4 v130, s[72:73]
	s_waitcnt vmcnt(8)
	s_waitcnt lgkmcnt(0)
	s_barrier
	s_setprio 1
	s_waitcnt lgkmcnt(6)
	v_mfma_scale_f32_16x16x128_f8f6f4 v[62:65], v[140:147], v[66:73], v[62:65], v200, v200 op_sel_hi:[0,0,0]
	v_mfma_scale_f32_16x16x128_f8f6f4 v[58:61], v[148:155], v[66:73], v[58:61], v200, v200 op_sel_hi:[0,0,0]
	s_waitcnt lgkmcnt(4)
	v_mfma_scale_f32_16x16x128_f8f6f4 v[50:53], v[140:147], v[74:81], v[50:53], v200, v200 op_sel_hi:[0,0,0]
	v_mfma_scale_f32_16x16x128_f8f6f4 v[210:213], v[148:155], v[74:81], v[42:45], v200, v200 op_sel_hi:[0,0,0]
	s_waitcnt lgkmcnt(2)
	v_mfma_scale_f32_16x16x128_f8f6f4 v[214:217], v[140:147], v[82:89], v[34:37], v200, v200 op_sel_hi:[0,0,0]
	v_mfma_scale_f32_16x16x128_f8f6f4 v[218:221], v[148:155], v[82:89], v[26:29], v200, v200 op_sel_hi:[0,0,0]
	s_waitcnt lgkmcnt(0)
	v_mfma_scale_f32_16x16x128_f8f6f4 v[222:225], v[140:147], v[90:97], v[18:21], v200, v200 op_sel_hi:[0,0,0]
	v_mfma_scale_f32_16x16x128_f8f6f4 v[226:229], v[148:155], v[90:97], v[10:13], v200, v200 op_sel_hi:[0,0,0]
	s_setprio 0
	s_setprio 1
	v_mfma_scale_f32_16x16x128_f8f6f4 v[54:57], v[156:163], v[66:73], v[54:57], v200, v200 op_sel_hi:[0,0,0]
	v_mfma_scale_f32_16x16x128_f8f6f4 v[230:233], v[164:171], v[66:73], v[46:49], v200, v200 op_sel_hi:[0,0,0]
	v_mfma_scale_f32_16x16x128_f8f6f4 v[234:237], v[156:163], v[74:81], v[38:41], v200, v200 op_sel_hi:[0,0,0]
	v_mfma_scale_f32_16x16x128_f8f6f4 v[238:241], v[164:171], v[74:81], v[30:33], v200, v200 op_sel_hi:[0,0,0]
	v_mfma_scale_f32_16x16x128_f8f6f4 v[242:245], v[156:163], v[82:89], v[22:25], v200, v200 op_sel_hi:[0,0,0]
	v_mfma_scale_f32_16x16x128_f8f6f4 v[246:249], v[164:171], v[82:89], v[14:17], v200, v200 op_sel_hi:[0,0,0]
	v_mfma_scale_f32_16x16x128_f8f6f4 v[250:253], v[156:163], v[90:97], v[6:9], v200, v200 op_sel_hi:[0,0,0]
	v_mfma_scale_f32_16x16x128_f8f6f4 v[202:205], v[164:171], v[90:97], v[2:5], v200, v200 op_sel_hi:[0,0,0]
	s_setprio 0
	s_barrier
	v_add_u32_e32 v10, 0x18000, v137
	v_add_u32_e32 v18, 0x1c000, v137
	s_nop 2
	ds_read_b128 v[2:5], v10
	ds_read_b128 v[6:9], v10 offset:16
	ds_read_b128 v[14:17], v10 offset:2064
	ds_read_b128 v[10:13], v10 offset:2048
	ds_read_b128 v[140:143], v18
	ds_read_b128 v[144:147], v18 offset:16
	ds_read_b128 v[152:155], v18 offset:2064
	ds_read_b128 v[148:151], v18 offset:2048
	ds_read_b128 v[18:21], v138 offset:32768
	ds_read_b128 v[22:25], v138 offset:32784
	ds_read_b128 v[30:33], v138 offset:34832
	ds_read_b128 v[26:29], v138 offset:34816
	ds_read_b128 v[38:41], v138 offset:36880
	ds_read_b128 v[34:37], v138 offset:36864
	ds_read_b128 v[46:49], v138 offset:38928
	ds_read_b128 v[42:45], v138 offset:38912
	s_add_u32 s72, s96, 0x70000
	s_addc_u32 s73, s97, 0
	s_mov_b32 m0, s21
	s_nop 0
	global_load_lds_dwordx4 v130, s[72:73]
	s_add_u32 s72, s72, 0x38000
	s_addc_u32 s73, s73, 0
	s_mov_b32 m0, s25
	s_nop 0
	global_load_lds_dwordx4 v130, s[72:73]
	s_waitcnt vmcnt(8)
	s_waitcnt lgkmcnt(0)
	s_barrier
	s_setprio 1
	s_waitcnt lgkmcnt(6)
	v_mfma_scale_f32_16x16x128_f8f6f4 v[126:129], v[2:9], v[18:25], v[126:129], v200, v200 op_sel_hi:[0,0,0]
	v_mfma_scale_f32_16x16x128_f8f6f4 v[122:125], v[10:17], v[18:25], v[122:125], v200, v200 op_sel_hi:[0,0,0]
	s_waitcnt lgkmcnt(4)
	v_mfma_scale_f32_16x16x128_f8f6f4 v[114:117], v[2:9], v[26:33], v[114:117], v200, v200 op_sel_hi:[0,0,0]
	v_mfma_scale_f32_16x16x128_f8f6f4 v[106:109], v[10:17], v[26:33], v[106:109], v200, v200 op_sel_hi:[0,0,0]
	s_waitcnt lgkmcnt(2)
	v_mfma_scale_f32_16x16x128_f8f6f4 v[98:101], v[2:9], v[34:41], v[98:101], v200, v200 op_sel_hi:[0,0,0]
	v_mfma_scale_f32_16x16x128_f8f6f4 v[90:93], v[10:17], v[34:41], v[132:135], v200, v200 op_sel_hi:[0,0,0]
	s_waitcnt lgkmcnt(0)
	v_mfma_scale_f32_16x16x128_f8f6f4 v[82:85], v[2:9], v[42:49], v[188:191], v200, v200 op_sel_hi:[0,0,0]
	v_mfma_scale_f32_16x16x128_f8f6f4 v[74:77], v[10:17], v[42:49], v[196:199], v200, v200 op_sel_hi:[0,0,0]
	s_setprio 0
	s_setprio 1
	v_mfma_scale_f32_16x16x128_f8f6f4 v[118:121], v[140:147], v[18:25], v[118:121], v200, v200 op_sel_hi:[0,0,0]
	v_mfma_scale_f32_16x16x128_f8f6f4 v[110:113], v[148:155], v[18:25], v[110:113], v200, v200 op_sel_hi:[0,0,0]
	v_mfma_scale_f32_16x16x128_f8f6f4 v[102:105], v[140:147], v[26:33], v[102:105], v200, v200 op_sel_hi:[0,0,0]
	v_mfma_scale_f32_16x16x128_f8f6f4 v[94:97], v[148:155], v[26:33], v[172:175], v200, v200 op_sel_hi:[0,0,0]
	v_mfma_scale_f32_16x16x128_f8f6f4 v[86:89], v[140:147], v[34:41], v[176:179], v200, v200 op_sel_hi:[0,0,0]
	v_mfma_scale_f32_16x16x128_f8f6f4 v[78:81], v[148:155], v[34:41], v[180:183], v200, v200 op_sel_hi:[0,0,0]
	v_mfma_scale_f32_16x16x128_f8f6f4 v[70:73], v[140:147], v[42:49], v[184:187], v200, v200 op_sel_hi:[0,0,0]
	v_mfma_scale_f32_16x16x128_f8f6f4 v[66:69], v[148:155], v[42:49], v[206:209], v200, v200 op_sel_hi:[0,0,0]
	s_setprio 0
	s_barrier
	s_add_u32 s72, s94, 0x80
	s_addc_u32 s73, s95, 0
	ds_read_b128 v[156:159], v138 offset:49152
	ds_read_b128 v[160:163], v138 offset:49168
	ds_read_b128 v[168:171], v138 offset:51216
	ds_read_b128 v[164:167], v138 offset:51200
	ds_read_b128 v[176:179], v138 offset:53264
	ds_read_b128 v[172:175], v138 offset:53248
	ds_read_b128 v[184:187], v138 offset:55312
	ds_read_b128 v[180:183], v138 offset:55296
	s_mov_b32 m0, s26
	s_nop 0
	global_load_lds_dwordx4 v131, s[72:73]
	s_add_u32 s72, s72, 0x38000
	s_addc_u32 s73, s73, 0
	s_mov_b32 m0, s30
	s_nop 0
	global_load_lds_dwordx4 v131, s[72:73]
	s_add_u32 s72, s94, 0x70080
	s_addc_u32 s73, s95, 0
	s_mov_b32 m0, s34
	s_nop 0
	global_load_lds_dwordx4 v131, s[72:73]
	s_add_u32 s72, s72, 0x38000
	s_addc_u32 s73, s73, 0
	s_mov_b32 m0, s42
	s_nop 0
	global_load_lds_dwordx4 v131, s[72:73]
	s_add_u32 s72, s78, 0x38000
	s_mov_b32 m0, s31
	s_nop 0
	global_load_lds_dwordx4 v130, s[78:79]
	s_addc_u32 s73, s79, 0
	s_mov_b32 m0, s33
	s_nop 0
	global_load_lds_dwordx4 v130, s[72:73]
	s_waitcnt vmcnt(8)
	s_waitcnt lgkmcnt(0)
	s_barrier
	s_setprio 1
	s_waitcnt lgkmcnt(6)
	v_mfma_scale_f32_16x16x128_f8f6f4 v[62:65], v[2:9], v[156:163], v[62:65], v200, v200 op_sel_hi:[0,0,0]
	v_mfma_scale_f32_16x16x128_f8f6f4 v[58:61], v[10:17], v[156:163], v[58:61], v200, v200 op_sel_hi:[0,0,0]
	s_waitcnt lgkmcnt(4)
	v_mfma_scale_f32_16x16x128_f8f6f4 v[50:53], v[2:9], v[164:171], v[50:53], v200, v200 op_sel_hi:[0,0,0]
	v_mfma_scale_f32_16x16x128_f8f6f4 v[42:45], v[10:17], v[164:171], v[210:213], v200, v200 op_sel_hi:[0,0,0]
	s_waitcnt lgkmcnt(2)
	v_mfma_scale_f32_16x16x128_f8f6f4 v[34:37], v[2:9], v[172:179], v[214:217], v200, v200 op_sel_hi:[0,0,0]
	v_mfma_scale_f32_16x16x128_f8f6f4 v[26:29], v[10:17], v[172:179], v[218:221], v200, v200 op_sel_hi:[0,0,0]
	s_waitcnt lgkmcnt(0)
	v_mfma_scale_f32_16x16x128_f8f6f4 v[18:21], v[2:9], v[180:187], v[222:225], v200, v200 op_sel_hi:[0,0,0]
	v_mfma_scale_f32_16x16x128_f8f6f4 v[10:13], v[10:17], v[180:187], v[226:229], v200, v200 op_sel_hi:[0,0,0]
	s_setprio 0
	s_setprio 1
	v_mfma_scale_f32_16x16x128_f8f6f4 v[54:57], v[140:147], v[156:163], v[54:57], v200, v200 op_sel_hi:[0,0,0]
	v_mfma_scale_f32_16x16x128_f8f6f4 v[46:49], v[148:155], v[156:163], v[230:233], v200, v200 op_sel_hi:[0,0,0]
	v_mfma_scale_f32_16x16x128_f8f6f4 v[38:41], v[140:147], v[164:171], v[234:237], v200, v200 op_sel_hi:[0,0,0]
	v_mfma_scale_f32_16x16x128_f8f6f4 v[30:33], v[148:155], v[164:171], v[238:241], v200, v200 op_sel_hi:[0,0,0]
	v_mfma_scale_f32_16x16x128_f8f6f4 v[22:25], v[140:147], v[172:179], v[242:245], v200, v200 op_sel_hi:[0,0,0]
	v_mfma_scale_f32_16x16x128_f8f6f4 v[14:17], v[148:155], v[172:179], v[246:249], v200, v200 op_sel_hi:[0,0,0]
	v_mfma_scale_f32_16x16x128_f8f6f4 v[6:9], v[140:147], v[180:187], v[250:253], v200, v200 op_sel_hi:[0,0,0]
	v_mfma_scale_f32_16x16x128_f8f6f4 v[2:5], v[148:155], v[180:187], v[202:205], v200, v200 op_sel_hi:[0,0,0]
	s_setprio 0
	s_barrier
	s_add_i32 s40, s40, 2
	s_add_u32 s38, s38, 0x100
	s_addc_u32 s39, s39, 0
	s_add_u32 s92, s92, 0x100
	s_addc_u32 s93, s93, 0
	s_cmp_gt_u32 s40, 25
	s_cbranch_scc0 .LBB0_1339
	s_and_b64 vcc, exec, s[84:85]
	s_cbranch_vccz .LBB0_1342
	s_barrier

.LBB0_1357:
	s_xor_b64 s[68:69], s[40:41], -1
	s_andn2_b64 vcc, exec, s[38:39]
	s_cbranch_vccnz .LBB0_1398
	v_bfe_i32 v5, v2, 27, 1
	v_lshlrev_b32_e32 v3, 4, v2
	v_lshrrev_b32_e32 v5, 22, v5
	v_add_u32_e32 v5, v3, v5
	v_and_b32_e32 v5, 0xfffffc00, v5
	v_ashrrev_i32_e32 v4, 31, v2
	v_sub_u32_e32 v5, v3, v5
	v_lshrrev_b32_e32 v4, 26, v4
	v_lshrrev_b32_e32 v6, 4, v5
	v_add_u32_e32 v4, v2, v4
	v_bitop3_b32 v6, v6, v5, 32 bitop3:0x6c
	v_ashrrev_i32_e32 v5, 31, v5
	v_ashrrev_i32_e32 v4, 6, v4
	v_lshrrev_b32_e32 v5, 26, v5
	v_lshlrev_b32_e32 v7, 3, v4
	v_add_u32_e32 v5, v6, v5
	v_and_b32_e32 v7, -16, v7
	v_ashrrev_i32_e32 v5, 6, v5
	v_add_u32_e32 v206, v5, v7
	v_mul_i32_i24_e32 v7, 64, v5
	v_sub_u32_e32 v6, v6, v7
	v_mov_b32_e32 v9, 1
	v_lshlrev_b32_e32 v4, 5, v4
	v_ashrrev_i16_sdwa v6, v9, sext(v6) dst_sel:DWORD dst_unused:UNUSED_PAD src0_sel:DWORD src1_sel:BYTE_0
	v_and_b32_e32 v4, 32, v4
	v_bfe_i32 v6, v6, 0, 16
	v_add_u32_e32 v3, 0x2000, v3
	v_add_lshl_u32 v207, v4, v6, 1
	v_ashrrev_i32_e32 v4, 31, v3
	v_lshlrev_b32_e32 v7, 1, v206
	v_lshrrev_b32_e32 v8, 2, v206
	v_and_b32_e32 v5, 3, v5
	s_mov_b32 s0, 0x3fffe0
	v_lshrrev_b32_e32 v4, 22, v4
	v_and_b32_e32 v7, 24, v7
	v_and_b32_e32 v8, 4, v8
	v_and_or_b32 v5, v206, s0, v5
	v_add_u32_e32 v4, v3, v4
	v_or3_b32 v5, v5, v8, v7
	v_ashrrev_i32_e32 v4, 10, v4
	v_lshl_add_u32 v208, v5, 10, v207
	v_mul_i32_i24_e32 v5, 0x400, v4
	v_sub_u32_e32 v3, v3, v5
	v_lshrrev_b32_e32 v5, 4, v3
	v_bitop3_b32 v3, v5, v3, 32 bitop3:0x6c
	v_lshlrev_b32_e32 v5, 3, v4
	v_and_b32_e32 v6, -16, v5
	v_ashrrev_i32_e32 v5, 31, v3
	v_lshrrev_b32_e32 v5, 26, v5
	v_add_u32_e32 v5, v3, v5
	v_ashrrev_i32_e32 v7, 6, v5
	v_and_b32_e32 v5, 0xc0, v5
	v_sub_u32_e32 v3, v3, v5
	s_lshl_b32 s0, s14, 10
	v_lshlrev_b32_e32 v4, 5, v4
	v_ashrrev_i16_sdwa v3, v9, sext(v3) dst_sel:DWORD dst_unused:UNUSED_PAD src0_sel:DWORD src1_sel:BYTE_0
	s_add_i32 s51, s0, 0
	s_lshl_b32 s0, s96, 15
	s_lshl_b32 s1, s97, 8
	v_and_b32_e32 v4, 32, v4
	v_bfe_i32 v3, v3, 0, 16
	s_add_i32 s1, s1, s0
	v_add_lshl_u32 v209, v4, v3, 1
	v_add_u32_e32 v4, s1, v206
	v_ashrrev_i32_e32 v5, 31, v4
	v_lshl_add_u64 v[4:5], v[4:5], 2, s[56:57]
	v_add_u32_e32 v210, v7, v6
	global_load_dword v3, v[4:5], off
	global_load_dword v8, v[4:5], off offset:512
	v_add_u32_e32 v4, s1, v210
	v_ashrrev_i32_e32 v5, 31, v4
	v_lshl_add_u64 v[4:5], v[4:5], 2, s[56:57]
	global_load_dword v6, v[4:5], off
	s_nop 0
	global_load_dword v4, v[4:5], off offset:512
	s_ashr_i32 s79, s78, 31
	s_ashr_i32 s31, s25, 8
	s_lshl_b64 s[0:1], s[78:79], 18
	s_add_u32 s78, s22, s0
	s_addc_u32 s79, s23, s1
	s_add_i32 s48, s51, 0x10000
	s_mov_b32 m0, s48
	s_nop 0
	global_load_lds_dwordx4 v208, s[78:79]
	s_add_u32 s0, s78, 0x10000
	s_addc_u32 s1, s79, 0
	s_add_i32 s49, s51, 0x12000
	s_mov_b32 m0, s49
	s_nop 0
	global_load_lds_dwordx4 v208, s[0:1]
	s_add_u32 s0, s78, 0x20000
	s_addc_u32 s1, s79, 0
	s_add_i32 s26, s51, 0x14000
	s_mov_b32 m0, s26
	s_nop 0
	global_load_lds_dwordx4 v208, s[0:1]
	s_add_u32 s4, s0, 0x10000
	s_addc_u32 s5, s1, 0
	s_add_i32 s0, s51, 0x16000
	s_mov_b32 m0, s0
	s_nop 0
	global_load_lds_dwordx4 v208, s[4:5]
	s_add_i32 s16, s51, 0x4000
	s_add_i32 s17, s51, 0x6000
	v_writelane_b32 v255, s46, 43
	v_mov_b32_e32 v201, 1
	s_waitcnt vmcnt(3)
	v_lshl_add_u32 v211, v3, 10, v207
	s_mov_b32 m0, s51
	s_nop 0
	global_load_lds_dwordx4 v211, s[62:63]
	s_add_i32 s1, s51, 0x2000
	s_waitcnt vmcnt(2)
	v_lshl_add_u32 v212, v8, 10, v207
	s_waitcnt vmcnt(1)
	v_lshl_add_u32 v213, v6, 10, v209
	s_mov_b32 m0, s1
	s_nop 0
	global_load_lds_dwordx4 v213, s[62:63]
	s_waitcnt vmcnt(0)
	v_lshl_add_u32 v214, v4, 10, v209
	s_mov_b32 m0, s16
	s_nop 0
	global_load_lds_dwordx4 v212, s[62:63]
	s_cmp_eq_u32 s31, 1
	s_mov_b32 m0, s17
	s_nop 0
	global_load_lds_dwordx4 v214, s[62:63]
	s_cselect_b64 s[80:81], -1, 0
	s_cmp_lg_u32 s31, 1
	s_cbranch_scc1 .LBB0_1360
	s_barrier
.LBB0_1360:
	s_bitcmp0_b32 s35, 0
	v_readlane_b32 s4, v254, 51
	v_readlane_b32 s5, v254, 53
	s_cselect_b32 s4, s4, s5
	v_readlane_b32 s5, v254, 50
	v_readlane_b32 s15, v254, 52
	v_and_b32_e32 v3, 15, v2
	v_lshlrev_b32_e32 v4, 1, v2
	v_lshlrev_b32_e32 v5, 5, v2
	v_lshlrev_b32_e32 v2, 2, v2
	s_cselect_b32 s5, s5, s15
	s_and_b32 s33, s14, 3
	v_lshlrev_b32_e32 v3, 6, v3
	v_and_b32_e32 v4, 32, v4
	v_and_b32_e32 v2, 32, v2
	v_bitop3_b32 v2, v4, v2, v3 bitop3:0x36
	s_movk_i32 s14, 0x400
	s_add_u32 s38, s78, 0x80
	v_and_or_b32 v2, v5, s14, v2
	s_addc_u32 s39, s79, 0
	s_add_i32 s14, s51, 0x18000
	s_waitcnt vmcnt(2)
	s_barrier
	s_mov_b32 m0, s14
	s_nop 0
	global_load_lds_dwordx4 v208, s[38:39]
	s_add_u32 s38, s38, 0x10000
	s_addc_u32 s39, s39, 0
	s_add_i32 s15, s51, 0x1a000
	s_mov_b32 m0, s15
	s_nop 0
	global_load_lds_dwordx4 v208, s[38:39]
	v_readlane_b32 s38, v254, 58
	s_add_i32 s34, s51, 0x8000
	v_readlane_b32 s39, v254, 59
	s_nop 2
	s_mov_b32 m0, s34
	s_nop 0
	global_load_lds_dwordx4 v211, s[38:39]
	s_add_i32 s19, s51, 0xa000
	s_mov_b32 m0, s19
	s_nop 0
	global_load_lds_dwordx4 v213, s[38:39]
	s_add_u32 s38, s78, 0x20080
	s_addc_u32 s39, s79, 0
	s_add_i32 s64, s51, 0x1c000
	s_mov_b32 m0, s64
	s_nop 0
	global_load_lds_dwordx4 v208, s[38:39]
	s_add_u32 s38, s38, 0x10000
	s_addc_u32 s39, s39, 0
	s_add_i32 s65, s51, 0x1e000
	s_mov_b32 m0, s65
	s_nop 0
	global_load_lds_dwordx4 v208, s[38:39]
	s_add_i32 s30, s51, 0xc000
	s_cmpk_lt_u32 s25, 0x100
	s_cselect_b64 s[82:83], -1, 0
	s_sub_i32 s61, 0x100, s21
	v_lshl_or_b32 v3, s31, 13, v2
	v_lshl_or_b32 v2, s33, 12, v2
	s_lshl_b32 s25, s33, 5
	s_mul_i32 s33, s61, 7
	s_ashr_i32 s33, s33, 1
	s_sub_i32 s33, 0xe80, s33
	s_lshl_b32 s31, s31, 6
	s_add_i32 s60, s51, 0xe000
	s_lshr_b32 s33, s33, 8
	s_cmp_ge_i32 s52, s21
	s_cselect_b64 s[84:85], -1, 0
	s_sub_i32 s72, s67, s21
	s_sub_i32 s43, s52, s21
	s_ashr_i32 s37, s72, 31
	s_mul_i32 s38, s72, 3
	v_writelane_b32 v255, s37, 44
	s_mul_hi_i32 s37, s72, 3
	s_add_u32 s38, s38, s52
	v_writelane_b32 v255, s38, 45
	s_addc_u32 s37, s37, s53
	v_writelane_b32 v255, s37, 46
	s_ashr_i32 s37, s43, 31
	s_cmp_lg_u32 s21, 0
	s_cselect_b64 s[86:87], -1, 0
	s_and_b64 s[38:39], s[86:87], exec
	s_cselect_b32 s55, s33, 14
	s_sub_i32 s73, 14, s55
	s_cmp_lg_u32 s55, 14
	s_cselect_b64 s[38:39], -1, 0
	s_abs_i32 s33, s73
	v_cvt_f32_u32_e32 v4, s33
	v_writelane_b32 v255, s37, 47
	v_writelane_b32 v255, s38, 48
	s_mul_i32 s21, s73, s21
	v_rcp_iflag_f32_e32 v4, v4
	v_writelane_b32 v255, s39, 49
	v_writelane_b32 v255, s21, 50
	s_ashr_i32 s21, s73, 31
	v_mul_f32_e32 v4, 0x4f7ffffe, v4
	v_cvt_u32_f32_e32 v4, v4
	v_writelane_b32 v255, s21, 51
	s_sub_i32 s21, 0, s33
	s_waitcnt vmcnt(6)
	v_readfirstlane_b32 s38, v4
	s_mul_i32 s21, s21, s38
	s_mul_hi_u32 s21, s38, s21
	s_add_i32 s21, s38, s21
	s_mov_b32 s46, 0
	s_mov_b32 s37, s50
	v_writelane_b32 v255, s21, 52
	v_add_u32_e32 v215, 0, v2
	v_add_u32_e32 v216, 0, v3
	s_barrier
	s_branch .LBB0_1363

.LBB0_1387:
	v_add_u32_e32 v2, 0x10000, v215
	v_add_u32_e32 v10, 0x14000, v215
	ds_read_b128 v[18:21], v2
	ds_read_b128 v[22:25], v2 offset:16
	ds_read_b128 v[30:33], v2 offset:2064
	ds_read_b128 v[26:29], v2 offset:2048
	ds_read_b128 v[2:5], v10
	ds_read_b128 v[6:9], v10 offset:16
	ds_read_b128 v[14:17], v10 offset:2064
	ds_read_b128 v[10:13], v10 offset:2048
	s_cmp_eq_u32 s88, 4
	s_cselect_b64 s[40:41], -1, 0
	ds_read_b128 v[58:61], v216
	ds_read_b128 v[62:65], v216 offset:16
	ds_read_b128 v[54:57], v216 offset:2064
	ds_read_b128 v[50:53], v216 offset:2048
	ds_read_b128 v[46:49], v216 offset:4112
	ds_read_b128 v[42:45], v216 offset:4096
	ds_read_b128 v[38:41], v216 offset:6160
	ds_read_b128 v[34:37], v216 offset:6144
	s_add_u32 s38, s62, s78
	s_addc_u32 s39, s63, s79
	s_add_u32 s38, s38, 0x80
	s_addc_u32 s39, s39, 0
	s_mov_b32 m0, s30
	s_nop 0
	global_load_lds_dwordx4 v212, s[38:39]
	s_nop 0
	s_mov_b32 m0, s60
	s_nop 0
	global_load_lds_dwordx4 v214, s[38:39]
	s_and_b64 s[38:39], s[92:93], s[40:41]
	s_and_b64 s[38:39], s[38:39], s[96:97]
	s_andn2_b64 vcc, exec, s[38:39]
	s_cbranch_vccnz .LBB0_1389
	global_load_dword v194, v[196:197], off
	global_load_dword v202, v[196:197], off offset:512
	global_load_dword v203, v[198:199], off
	global_load_dword v204, v[198:199], off offset:512
	s_waitcnt vmcnt(3)
	v_lshl_add_u32 v211, v194, 10, v207
	s_waitcnt vmcnt(2)
	v_lshl_add_u32 v212, v202, 10, v207
	s_waitcnt vmcnt(1)
	v_lshl_add_u32 v213, v203, 10, v209
	s_waitcnt vmcnt(0)
	v_lshl_add_u32 v214, v204, 10, v209
.LBB0_1389:
	s_add_u32 vcc_lo, s78, 0x100
	s_addc_u32 vcc_hi, s79, 0
	s_and_b64 s[38:39], s[40:41], exec
	s_cselect_b32 s76, 0, vcc_lo
	s_add_u32 s78, s91, s78
	s_addc_u32 s79, s46, s79
	s_waitcnt vmcnt(8)
	s_and_b64 s[38:39], s[40:41], exec
	s_waitcnt lgkmcnt(0)
	s_cselect_b32 s78, s94, s78
	s_cselect_b32 s79, s95, s79
	s_add_u32 s40, s78, 0x80
	s_addc_u32 s41, s79, 0
	s_barrier
	s_setprio 1
	s_waitcnt lgkmcnt(6)
	v_mfma_scale_f32_16x16x128_f8f6f4 v[190:193], v[18:25], v[58:65], v[190:193], v200, v200 op_sel_hi:[0,0,0]
	v_mfma_scale_f32_16x16x128_f8f6f4 v[182:185], v[26:33], v[58:65], v[182:185], v200, v200 op_sel_hi:[0,0,0]
	s_waitcnt lgkmcnt(4)
	v_mfma_scale_f32_16x16x128_f8f6f4 v[174:177], v[18:25], v[50:57], v[174:177], v200, v200 op_sel_hi:[0,0,0]
	v_mfma_scale_f32_16x16x128_f8f6f4 v[166:169], v[26:33], v[50:57], v[166:169], v200, v200 op_sel_hi:[0,0,0]
	s_waitcnt lgkmcnt(2)
	v_mfma_scale_f32_16x16x128_f8f6f4 v[158:161], v[18:25], v[42:49], v[158:161], v200, v200 op_sel_hi:[0,0,0]
	v_mfma_scale_f32_16x16x128_f8f6f4 v[150:153], v[26:33], v[42:49], v[150:153], v200, v200 op_sel_hi:[0,0,0]
	s_waitcnt lgkmcnt(0)
	v_mfma_scale_f32_16x16x128_f8f6f4 v[142:145], v[18:25], v[34:41], v[142:145], v200, v200 op_sel_hi:[0,0,0]
	v_mfma_scale_f32_16x16x128_f8f6f4 v[134:137], v[26:33], v[34:41], v[134:137], v200, v200 op_sel_hi:[0,0,0]
	s_setprio 0
	s_setprio 1
	v_mfma_scale_f32_16x16x128_f8f6f4 v[186:189], v[2:9], v[58:65], v[186:189], v200, v200 op_sel_hi:[0,0,0]
	v_mfma_scale_f32_16x16x128_f8f6f4 v[178:181], v[10:17], v[58:65], v[178:181], v200, v200 op_sel_hi:[0,0,0]
	v_mfma_scale_f32_16x16x128_f8f6f4 v[170:173], v[2:9], v[50:57], v[170:173], v200, v200 op_sel_hi:[0,0,0]
	v_mfma_scale_f32_16x16x128_f8f6f4 v[162:165], v[10:17], v[50:57], v[162:165], v200, v200 op_sel_hi:[0,0,0]
	v_mfma_scale_f32_16x16x128_f8f6f4 v[154:157], v[2:9], v[42:49], v[154:157], v200, v200 op_sel_hi:[0,0,0]
	v_mfma_scale_f32_16x16x128_f8f6f4 v[146:149], v[10:17], v[42:49], v[146:149], v200, v200 op_sel_hi:[0,0,0]
	v_mfma_scale_f32_16x16x128_f8f6f4 v[138:141], v[2:9], v[34:41], v[138:141], v200, v200 op_sel_hi:[0,0,0]
	v_mfma_scale_f32_16x16x128_f8f6f4 v[130:133], v[10:17], v[34:41], v[130:133], v200, v200 op_sel_hi:[0,0,0]
	s_setprio 0
	s_barrier
	ds_read_b128 v[34:37], v216 offset:16384
	ds_read_b128 v[38:41], v216 offset:16400
	ds_read_b128 v[46:49], v216 offset:18448
	ds_read_b128 v[42:45], v216 offset:18432
	ds_read_b128 v[54:57], v216 offset:20496
	ds_read_b128 v[50:53], v216 offset:20480
	ds_read_b128 v[62:65], v216 offset:22544
	ds_read_b128 v[58:61], v216 offset:22528
	s_mov_b32 m0, s48
	s_nop 0
	global_load_lds_dwordx4 v208, s[78:79]
	s_add_u32 s38, s78, 0x10000
	s_addc_u32 s39, s79, 0
	s_mov_b32 m0, s49
	s_nop 0
	global_load_lds_dwordx4 v208, s[38:39]
	s_add_u32 s38, s78, 0x20000
	s_addc_u32 s39, s79, 0
	s_mov_b32 m0, s26
	s_nop 0
	global_load_lds_dwordx4 v208, s[38:39]
	s_add_u32 s38, s38, 0x10000
	s_addc_u32 s39, s39, 0
	s_mov_b32 m0, s0
	s_nop 0
	global_load_lds_dwordx4 v208, s[38:39]
	s_add_u32 s38, s62, s76
	s_addc_u32 s39, s63, 0
	s_mov_b32 m0, s51
	s_nop 0
	global_load_lds_dwordx4 v211, s[38:39]
	s_nop 0
	s_mov_b32 m0, s1
	s_nop 0
	global_load_lds_dwordx4 v213, s[38:39]
	s_waitcnt vmcnt(8)
	s_waitcnt lgkmcnt(0)
	s_barrier
	s_setprio 1
	s_waitcnt lgkmcnt(6)
	v_mfma_scale_f32_16x16x128_f8f6f4 v[126:129], v[18:25], v[34:41], v[126:129], v200, v200 op_sel_hi:[0,0,0]
	v_mfma_scale_f32_16x16x128_f8f6f4 v[118:121], v[26:33], v[34:41], v[118:121], v200, v200 op_sel_hi:[0,0,0]
	s_waitcnt lgkmcnt(4)
	v_mfma_scale_f32_16x16x128_f8f6f4 v[110:113], v[18:25], v[42:49], v[110:113], v200, v200 op_sel_hi:[0,0,0]
	v_mfma_scale_f32_16x16x128_f8f6f4 v[102:105], v[26:33], v[42:49], v[102:105], v200, v200 op_sel_hi:[0,0,0]
	s_waitcnt lgkmcnt(2)
	v_mfma_scale_f32_16x16x128_f8f6f4 v[94:97], v[18:25], v[50:57], v[94:97], v200, v200 op_sel_hi:[0,0,0]
	v_mfma_scale_f32_16x16x128_f8f6f4 v[86:89], v[26:33], v[50:57], v[86:89], v200, v200 op_sel_hi:[0,0,0]
	s_waitcnt lgkmcnt(0)
	v_mfma_scale_f32_16x16x128_f8f6f4 v[78:81], v[18:25], v[58:65], v[78:81], v200, v200 op_sel_hi:[0,0,0]
	v_mfma_scale_f32_16x16x128_f8f6f4 v[70:73], v[26:33], v[58:65], v[70:73], v200, v200 op_sel_hi:[0,0,0]
	s_setprio 0
	s_setprio 1
	v_mfma_scale_f32_16x16x128_f8f6f4 v[122:125], v[2:9], v[34:41], v[122:125], v200, v200 op_sel_hi:[0,0,0]
	v_mfma_scale_f32_16x16x128_f8f6f4 v[114:117], v[10:17], v[34:41], v[114:117], v200, v200 op_sel_hi:[0,0,0]
	v_mfma_scale_f32_16x16x128_f8f6f4 v[106:109], v[2:9], v[42:49], v[106:109], v200, v200 op_sel_hi:[0,0,0]
	v_mfma_scale_f32_16x16x128_f8f6f4 v[98:101], v[10:17], v[42:49], v[98:101], v200, v200 op_sel_hi:[0,0,0]
	v_mfma_scale_f32_16x16x128_f8f6f4 v[90:93], v[2:9], v[50:57], v[90:93], v200, v200 op_sel_hi:[0,0,0]
	v_mfma_scale_f32_16x16x128_f8f6f4 v[82:85], v[10:17], v[50:57], v[82:85], v200, v200 op_sel_hi:[0,0,0]
	v_mfma_scale_f32_16x16x128_f8f6f4 v[74:77], v[2:9], v[58:65], v[74:77], v200, v200 op_sel_hi:[0,0,0]
	v_mfma_scale_f32_16x16x128_f8f6f4 v[66:69], v[10:17], v[58:65], v[66:69], v200, v200 op_sel_hi:[0,0,0]
	s_setprio 0
	s_barrier
	v_add_u32_e32 v10, 0x18000, v215
	v_add_u32_e32 v26, 0x1c000, v215
	ds_read_b128 v[2:5], v10
	ds_read_b128 v[6:9], v10 offset:16
	ds_read_b128 v[14:17], v10 offset:2064
	ds_read_b128 v[10:13], v10 offset:2048
	ds_read_b128 v[18:21], v26
	ds_read_b128 v[22:25], v26 offset:16
	ds_read_b128 v[30:33], v26 offset:2064
	ds_read_b128 v[26:29], v26 offset:2048
	ds_read_b128 v[34:37], v216 offset:32768
	ds_read_b128 v[38:41], v216 offset:32784
	ds_read_b128 v[46:49], v216 offset:34832
	ds_read_b128 v[42:45], v216 offset:34816
	ds_read_b128 v[54:57], v216 offset:36880
	ds_read_b128 v[50:53], v216 offset:36864
	ds_read_b128 v[62:65], v216 offset:38928
	ds_read_b128 v[58:61], v216 offset:38912
	s_mov_b32 m0, s16
	s_nop 0
	global_load_lds_dwordx4 v212, s[38:39]
	s_nop 0
	s_mov_b32 m0, s17
	s_nop 0
	global_load_lds_dwordx4 v214, s[38:39]
	s_waitcnt vmcnt(8)
	s_waitcnt lgkmcnt(0)
	s_barrier
	s_setprio 1
	s_waitcnt lgkmcnt(6)
	v_mfma_scale_f32_16x16x128_f8f6f4 v[190:193], v[2:9], v[34:41], v[190:193], v200, v200 op_sel_hi:[0,0,0]
	v_mfma_scale_f32_16x16x128_f8f6f4 v[182:185], v[10:17], v[34:41], v[182:185], v200, v200 op_sel_hi:[0,0,0]
	s_waitcnt lgkmcnt(4)
	v_mfma_scale_f32_16x16x128_f8f6f4 v[174:177], v[2:9], v[42:49], v[174:177], v200, v200 op_sel_hi:[0,0,0]
	v_mfma_scale_f32_16x16x128_f8f6f4 v[166:169], v[10:17], v[42:49], v[166:169], v200, v200 op_sel_hi:[0,0,0]
	s_waitcnt lgkmcnt(2)
	v_mfma_scale_f32_16x16x128_f8f6f4 v[158:161], v[2:9], v[50:57], v[158:161], v200, v200 op_sel_hi:[0,0,0]
	v_mfma_scale_f32_16x16x128_f8f6f4 v[150:153], v[10:17], v[50:57], v[150:153], v200, v200 op_sel_hi:[0,0,0]
	s_waitcnt lgkmcnt(0)
	v_mfma_scale_f32_16x16x128_f8f6f4 v[142:145], v[2:9], v[58:65], v[142:145], v200, v200 op_sel_hi:[0,0,0]
	v_mfma_scale_f32_16x16x128_f8f6f4 v[134:137], v[10:17], v[58:65], v[134:137], v200, v200 op_sel_hi:[0,0,0]
	s_setprio 0
	s_setprio 1
	v_mfma_scale_f32_16x16x128_f8f6f4 v[186:189], v[18:25], v[34:41], v[186:189], v200, v200 op_sel_hi:[0,0,0]
	v_mfma_scale_f32_16x16x128_f8f6f4 v[178:181], v[26:33], v[34:41], v[178:181], v200, v200 op_sel_hi:[0,0,0]
	v_mfma_scale_f32_16x16x128_f8f6f4 v[170:173], v[18:25], v[42:49], v[170:173], v200, v200 op_sel_hi:[0,0,0]
	v_mfma_scale_f32_16x16x128_f8f6f4 v[162:165], v[26:33], v[42:49], v[162:165], v200, v200 op_sel_hi:[0,0,0]
	v_mfma_scale_f32_16x16x128_f8f6f4 v[154:157], v[18:25], v[50:57], v[154:157], v200, v200 op_sel_hi:[0,0,0]
	v_mfma_scale_f32_16x16x128_f8f6f4 v[146:149], v[26:33], v[50:57], v[146:149], v200, v200 op_sel_hi:[0,0,0]
	v_mfma_scale_f32_16x16x128_f8f6f4 v[138:141], v[18:25], v[58:65], v[138:141], v200, v200 op_sel_hi:[0,0,0]
	v_mfma_scale_f32_16x16x128_f8f6f4 v[130:133], v[26:33], v[58:65], v[130:133], v200, v200 op_sel_hi:[0,0,0]
	s_setprio 0
	s_barrier
	ds_read_b128 v[34:37], v216 offset:49152
	ds_read_b128 v[38:41], v216 offset:49168
	ds_read_b128 v[46:49], v216 offset:51216
	ds_read_b128 v[42:45], v216 offset:51200
	ds_read_b128 v[54:57], v216 offset:53264
	ds_read_b128 v[50:53], v216 offset:53248
	ds_read_b128 v[62:65], v216 offset:55312
	ds_read_b128 v[58:61], v216 offset:55296
	s_mov_b32 m0, s14
	s_nop 0
	global_load_lds_dwordx4 v208, s[40:41]
	s_add_u32 s40, s40, 0x10000
	s_addc_u32 s41, s41, 0
	s_mov_b32 m0, s15
	s_nop 0
	global_load_lds_dwordx4 v208, s[40:41]
	s_add_u32 s40, s78, 0x20080
	s_addc_u32 s41, s79, 0
	s_mov_b32 m0, s64
	s_nop 0
	global_load_lds_dwordx4 v208, s[40:41]
	s_add_u32 s40, s40, 0x10000
	s_addc_u32 s41, s41, 0
	s_mov_b32 m0, s65
	s_nop 0
	global_load_lds_dwordx4 v208, s[40:41]
	s_add_u32 s38, s38, 0x80
	s_addc_u32 s39, s39, 0
	s_mov_b32 m0, s34
	s_nop 0
	global_load_lds_dwordx4 v211, s[38:39]
	s_nop 0
	s_mov_b32 m0, s19
	s_nop 0
	global_load_lds_dwordx4 v213, s[38:39]
	s_waitcnt vmcnt(8)
	s_waitcnt lgkmcnt(0)
	s_barrier
	s_setprio 1
	s_waitcnt lgkmcnt(6)
	v_mfma_scale_f32_16x16x128_f8f6f4 v[126:129], v[2:9], v[34:41], v[126:129], v200, v200 op_sel_hi:[0,0,0]
	v_mfma_scale_f32_16x16x128_f8f6f4 v[118:121], v[10:17], v[34:41], v[118:121], v200, v200 op_sel_hi:[0,0,0]
	s_waitcnt lgkmcnt(4)
	v_mfma_scale_f32_16x16x128_f8f6f4 v[110:113], v[2:9], v[42:49], v[110:113], v200, v200 op_sel_hi:[0,0,0]
	v_mfma_scale_f32_16x16x128_f8f6f4 v[102:105], v[10:17], v[42:49], v[102:105], v200, v200 op_sel_hi:[0,0,0]
	s_waitcnt lgkmcnt(2)
	v_mfma_scale_f32_16x16x128_f8f6f4 v[94:97], v[2:9], v[50:57], v[94:97], v200, v200 op_sel_hi:[0,0,0]
	v_mfma_scale_f32_16x16x128_f8f6f4 v[86:89], v[10:17], v[50:57], v[86:89], v200, v200 op_sel_hi:[0,0,0]
	s_waitcnt lgkmcnt(0)
	v_mfma_scale_f32_16x16x128_f8f6f4 v[78:81], v[2:9], v[58:65], v[78:81], v200, v200 op_sel_hi:[0,0,0]
	v_mfma_scale_f32_16x16x128_f8f6f4 v[70:73], v[10:17], v[58:65], v[70:73], v200, v200 op_sel_hi:[0,0,0]
	s_setprio 0
	s_setprio 1
	v_mfma_scale_f32_16x16x128_f8f6f4 v[122:125], v[18:25], v[34:41], v[122:125], v200, v200 op_sel_hi:[0,0,0]
	v_mfma_scale_f32_16x16x128_f8f6f4 v[114:117], v[26:33], v[34:41], v[114:117], v200, v200 op_sel_hi:[0,0,0]
	v_mfma_scale_f32_16x16x128_f8f6f4 v[106:109], v[18:25], v[42:49], v[106:109], v200, v200 op_sel_hi:[0,0,0]
	v_mfma_scale_f32_16x16x128_f8f6f4 v[98:101], v[26:33], v[42:49], v[98:101], v200, v200 op_sel_hi:[0,0,0]
	v_mfma_scale_f32_16x16x128_f8f6f4 v[90:93], v[18:25], v[50:57], v[90:93], v200, v200 op_sel_hi:[0,0,0]
	v_mfma_scale_f32_16x16x128_f8f6f4 v[82:85], v[26:33], v[50:57], v[82:85], v200, v200 op_sel_hi:[0,0,0]
	v_mfma_scale_f32_16x16x128_f8f6f4 v[74:77], v[18:25], v[58:65], v[74:77], v200, v200 op_sel_hi:[0,0,0]
	v_mfma_scale_f32_16x16x128_f8f6f4 v[66:69], v[26:33], v[58:65], v[66:69], v200, v200 op_sel_hi:[0,0,0]
	s_setprio 0
	s_barrier
	s_add_i32 s88, s88, 2
	s_cmp_gt_u32 s88, 5
	s_cbranch_scc1 .LBB0_1391
	s_mov_b64 s[78:79], vcc
	s_branch .LBB0_1387
